# P12 last pass: gain vector loaded once, 2 rows x 16 pieces in flight with counted vmcnt; per-wave L2 writeback before the re-read removed (same-CU re-read, L1 invalidate kept)
# speedup vs baseline: 1.0420x; 1.0420x over previous
; #define P12_VISSUE(c_, i_, q_, D_X) do { _Pragma("unroll") for (int b = 0; b < 8; ++b) { const int idx = ((q_) * 8 + b) * 4 + eg; const unsigned ro = (unsigned)(c_) * 16384u + (unsigned)EL[(i_) * 128 + idx]; \
;           const v3u_ ld_ = *(const v3u_*)(V8 + (size_t)(ro * 192u + 12u * (unsigned)cl)); if (b & 1) D_X[b >> 1].hi = ld_; else D_X[b >> 1].lo = ld_; } } while (0)
; __device__ __forceinline__ void p12_peer(Frame& F) {
;     ...
;       v6u_ dA[4], dB[4];
;       P12_VISSUE(0, 0, 0, dA);
; _Pragma("nounroll")
;       for (int c = 0; c < 16; ++c) {
;           int lo_ = 16 * cl + 4 * eg; asm volatile("" : "+v"(lo_));
; _Pragma("nounroll")
;           for (int i = 0; i < 4; ++i) { const int t = F.gw + i * F.NGW;
;               f32x2 acc2[8];
; #pragma unroll
;               for (int m = 0; m < 8; ++m) acc2[m] = (f32x2){0.f, 0.f};
;               const v2u hb = *(const v2u*)(HN + ((size_t)t * D_ + (size_t)(unsigned)(256 * c + lo_)));
;               P12_VISSUE(c, i, 1, dB); asm volatile("" ::: "memory"); P12_VCOMP(i, 0, dA);
;               P12_VISSUE(c, i, 2, dA); asm volatile("" ::: "memory"); P12_VCOMP(i, 1, dB);
;               P12_VISSUE(c, i, 3, dB); asm volatile("" ::: "memory"); P12_VCOMP(i, 2, dA);
;               { const int in_ = i + 1 < 4 ? i + 1 : 0, cn_ = i + 1 < 4 ? c : (c + 1 < 16 ? c + 1 : 15); P12_VISSUE(cn_, in_, 0, dA); } asm volatile("" ::: "memory"); P12_VCOMP(i, 3, dB);
.LBB0_3403:
	v_add_u32_e32 v152, s28, v175
	ds_read_u16 v2, v152
	ds_read_u16 v3, v152 offset:8
	ds_read_u16 v4, v152 offset:16
	ds_read_u16 v5, v152 offset:24
	ds_read_u16 v6, v152 offset:32
	ds_read_u16 v7, v152 offset:40
	ds_read_u16 v8, v152 offset:48
	ds_read_u16 v9, v152 offset:56
	s_ashr_i32 s13, s12, 31
	s_lshl_b64 s[14:15], s[12:13], 13
	v_lshl_add_u64 v[0:1], v[164:165], 0, s[14:15]
	s_cmpk_eq_i32 s28, 0x300
	global_load_dwordx2 v[158:159], v[0:1], off
	s_cselect_b32 s30, 0, s23
	s_waitcnt lgkmcnt(7)
	v_add_u32_e32 v0, s21, v2
	v_lshl_add_u32 v179, s30, 1, v161
	s_waitcnt lgkmcnt(6)
	v_add_u32_e32 v2, s21, v3
	s_waitcnt lgkmcnt(5)
	v_add_u32_e32 v4, s21, v4
	s_waitcnt lgkmcnt(4)
	v_add_u32_e32 v10, s21, v5
	s_waitcnt lgkmcnt(3)
	v_add_u32_e32 v11, s21, v6
	s_waitcnt lgkmcnt(2)
	v_add_u32_e32 v12, s21, v7
	s_waitcnt lgkmcnt(1)
	v_add_u32_e32 v13, s21, v8
	s_waitcnt lgkmcnt(0)
	v_add_u32_e32 v14, s21, v9
	v_mad_u64_u32 v[0:1], s[30:31], v0, s16, v[160:161]
	v_mad_u64_u32 v[2:3], s[30:31], v2, s16, v[160:161]
	v_mad_u64_u32 v[4:5], s[30:31], v4, s16, v[160:161]
	v_mad_u64_u32 v[6:7], s[30:31], v10, s16, v[160:161]
	v_mad_u64_u32 v[8:9], s[30:31], v11, s16, v[160:161]
	v_mad_u64_u32 v[10:11], s[30:31], v12, s16, v[160:161]
	v_mad_u64_u32 v[12:13], s[30:31], v13, s16, v[160:161]
	v_mad_u64_u32 v[14:15], s[30:31], v14, s16, v[160:161]
	global_load_dwordx3 v[154:156], v0, s[2:3]
	global_load_dwordx3 v[220:222], v2, s[2:3]
	global_load_dwordx3 v[180:182], v4, s[2:3]
	global_load_dwordx3 v[224:226], v6, s[2:3]
	global_load_dwordx3 v[186:188], v8, s[2:3]
	global_load_dwordx3 v[228:230], v10, s[2:3]
	global_load_dwordx3 v[192:194], v12, s[2:3]
	global_load_dwordx3 v[232:234], v14, s[2:3]
	ds_read2_b32 v[166:167], v177 offset1:4
	ds_read2_b32 v[168:169], v177 offset0:8 offset1:12
	s_waitcnt vmcnt(10)
	ds_read2_b32 v[184:185], v177 offset0:16 offset1:20
	s_waitcnt vmcnt(9)
	ds_read2_b32 v[190:191], v177 offset0:24 offset1:28
	v_cvt_scalef32_pk32_f32_fp6 v[96:127], v[134:139], 1.0
	v_cvt_scalef32_pk32_f32_fp6 v[64:95], v[128:133], 1.0
	ds_read_u16 v129, v152 offset:64
	ds_read_u16 v131, v152 offset:72
	ds_read_u16 v132, v152 offset:80
	ds_read_u16 v133, v152 offset:88
	ds_read_u16 v134, v152 offset:96
	ds_read_u16 v135, v152 offset:104
	ds_read_u16 v136, v152 offset:112
	ds_read_u16 v137, v152 offset:120
	s_waitcnt lgkmcnt(11)
	v_pk_fma_f32 v[96:97], v[96:97], v[166:167], 0 op_sel_hi:[1,0,0]
	v_pk_fma_f32 v[98:99], v[98:99], v[166:167], 0 op_sel_hi:[1,0,0]
	v_pk_fma_f32 v[100:101], v[100:101], v[166:167], 0 op_sel_hi:[1,0,0]
	v_pk_fma_f32 v[102:103], v[102:103], v[166:167], 0 op_sel_hi:[1,0,0]
	v_pk_fma_f32 v[104:105], v[104:105], v[166:167], 0 op_sel_hi:[1,0,0]
	v_pk_fma_f32 v[106:107], v[106:107], v[166:167], 0 op_sel_hi:[1,0,0]
	v_pk_fma_f32 v[108:109], v[108:109], v[166:167], 0 op_sel_hi:[1,0,0]
	v_pk_fma_f32 v[110:111], v[110:111], v[166:167], 0 op_sel_hi:[1,0,0]
	v_mov_b32_e32 v128, v167
	s_waitcnt lgkmcnt(7)
	v_pk_fma_f32 v[96:97], v[112:113], v[128:129], v[96:97] op_sel_hi:[1,0,1]
	v_pk_fma_f32 v[98:99], v[114:115], v[128:129], v[98:99] op_sel_hi:[1,0,1]
	v_pk_fma_f32 v[100:101], v[116:117], v[128:129], v[100:101] op_sel_hi:[1,0,1]
	v_pk_fma_f32 v[102:103], v[118:119], v[128:129], v[102:103] op_sel_hi:[1,0,1]
	v_pk_fma_f32 v[104:105], v[120:121], v[128:129], v[104:105] op_sel_hi:[1,0,1]
	v_pk_fma_f32 v[106:107], v[122:123], v[128:129], v[106:107] op_sel_hi:[1,0,1]
	v_pk_fma_f32 v[108:109], v[124:125], v[128:129], v[108:109] op_sel_hi:[1,0,1]
	v_pk_fma_f32 v[110:111], v[126:127], v[128:129], v[110:111] op_sel_hi:[1,0,1]
	v_add_u32_e32 v112, s21, v129
	v_mov_b32_e32 v130, v169
	s_waitcnt lgkmcnt(6)
	v_add_u32_e32 v113, s21, v131
	s_waitcnt lgkmcnt(5)
	v_add_u32_e32 v114, s21, v132
	s_waitcnt lgkmcnt(4)
	v_add_u32_e32 v115, s21, v133
	s_waitcnt lgkmcnt(3)
	v_add_u32_e32 v116, s21, v134
	s_waitcnt lgkmcnt(2)
	v_add_u32_e32 v117, s21, v135
	s_waitcnt lgkmcnt(1)
	v_add_u32_e32 v118, s21, v136
	s_waitcnt lgkmcnt(0)
	v_add_u32_e32 v119, s21, v137
	v_pk_fma_f32 v[64:65], v[64:65], v[168:169], v[96:97] op_sel_hi:[1,0,1]
	v_pk_fma_f32 v[66:67], v[66:67], v[168:169], v[98:99] op_sel_hi:[1,0,1]
	v_pk_fma_f32 v[68:69], v[68:69], v[168:169], v[100:101] op_sel_hi:[1,0,1]
	v_pk_fma_f32 v[70:71], v[70:71], v[168:169], v[102:103] op_sel_hi:[1,0,1]
	v_pk_fma_f32 v[72:73], v[72:73], v[168:169], v[104:105] op_sel_hi:[1,0,1]
	v_pk_fma_f32 v[74:75], v[74:75], v[168:169], v[106:107] op_sel_hi:[1,0,1]
	v_pk_fma_f32 v[76:77], v[76:77], v[168:169], v[108:109] op_sel_hi:[1,0,1]
	v_pk_fma_f32 v[78:79], v[78:79], v[168:169], v[110:111] op_sel_hi:[1,0,1]
	v_mad_u64_u32 v[96:97], s[30:31], v112, s16, v[160:161]
	v_cvt_scalef32_pk32_f32_fp6 v[32:63], v[140:145], 1.0
	v_mad_u64_u32 v[98:99], s[30:31], v113, s16, v[160:161]
	v_mad_u64_u32 v[100:101], s[30:31], v114, s16, v[160:161]
	v_mad_u64_u32 v[102:103], s[30:31], v115, s16, v[160:161]
	v_mad_u64_u32 v[104:105], s[30:31], v116, s16, v[160:161]
	v_mad_u64_u32 v[106:107], s[30:31], v117, s16, v[160:161]
	v_mad_u64_u32 v[108:109], s[30:31], v118, s16, v[160:161]
	v_mad_u64_u32 v[110:111], s[30:31], v119, s16, v[160:161]
	v_pk_fma_f32 v[64:65], v[80:81], v[130:131], v[64:65] op_sel_hi:[1,0,1]
	v_pk_fma_f32 v[66:67], v[82:83], v[130:131], v[66:67] op_sel_hi:[1,0,1]
	v_pk_fma_f32 v[68:69], v[84:85], v[130:131], v[68:69] op_sel_hi:[1,0,1]
	v_pk_fma_f32 v[70:71], v[86:87], v[130:131], v[70:71] op_sel_hi:[1,0,1]
	v_pk_fma_f32 v[72:73], v[88:89], v[130:131], v[72:73] op_sel_hi:[1,0,1]
	v_pk_fma_f32 v[74:75], v[90:91], v[130:131], v[74:75] op_sel_hi:[1,0,1]
	v_pk_fma_f32 v[76:77], v[92:93], v[130:131], v[76:77] op_sel_hi:[1,0,1]
	v_pk_fma_f32 v[78:79], v[94:95], v[130:131], v[78:79] op_sel_hi:[1,0,1]
	global_load_dwordx3 v[198:200], v96, s[2:3]
	global_load_dwordx3 v[128:130], v98, s[2:3]
	global_load_dwordx3 v[204:206], v100, s[2:3]
	global_load_dwordx3 v[132:134], v102, s[2:3]
	global_load_dwordx3 v[210:212], v104, s[2:3]
	global_load_dwordx3 v[136:138], v106, s[2:3]
	global_load_dwordx3 v[216:218], v108, s[2:3]
	global_load_dwordx3 v[140:142], v110, s[2:3]
	v_mov_b32_e32 v144, v185
	v_pk_fma_f32 v[32:33], v[32:33], v[184:185], v[64:65] op_sel_hi:[1,0,1]
	v_pk_fma_f32 v[34:35], v[34:35], v[184:185], v[66:67] op_sel_hi:[1,0,1]
	v_pk_fma_f32 v[36:37], v[36:37], v[184:185], v[68:69] op_sel_hi:[1,0,1]
	v_pk_fma_f32 v[38:39], v[38:39], v[184:185], v[70:71] op_sel_hi:[1,0,1]
	v_pk_fma_f32 v[40:41], v[40:41], v[184:185], v[72:73] op_sel_hi:[1,0,1]
	v_pk_fma_f32 v[42:43], v[42:43], v[184:185], v[74:75] op_sel_hi:[1,0,1]
	v_pk_fma_f32 v[44:45], v[44:45], v[184:185], v[76:77] op_sel_hi:[1,0,1]
	v_pk_fma_f32 v[46:47], v[46:47], v[184:185], v[78:79] op_sel_hi:[1,0,1]
	v_cvt_scalef32_pk32_f32_fp6 v[0:31], v[146:151], 1.0
	v_pk_fma_f32 v[32:33], v[48:49], v[144:145], v[32:33] op_sel_hi:[1,0,1]
	v_pk_fma_f32 v[34:35], v[50:51], v[144:145], v[34:35] op_sel_hi:[1,0,1]
	v_pk_fma_f32 v[36:37], v[52:53], v[144:145], v[36:37] op_sel_hi:[1,0,1]
	v_pk_fma_f32 v[38:39], v[54:55], v[144:145], v[38:39] op_sel_hi:[1,0,1]
	v_pk_fma_f32 v[40:41], v[56:57], v[144:145], v[40:41] op_sel_hi:[1,0,1]
	v_pk_fma_f32 v[42:43], v[58:59], v[144:145], v[42:43] op_sel_hi:[1,0,1]
	v_pk_fma_f32 v[44:45], v[60:61], v[144:145], v[44:45] op_sel_hi:[1,0,1]
	v_pk_fma_f32 v[46:47], v[62:63], v[144:145], v[46:47] op_sel_hi:[1,0,1]
	s_waitcnt vmcnt(16)
	v_lshlrev_b32_e32 v167, 16, v159
	v_lshlrev_b32_e32 v166, 16, v158
	v_and_b32_e32 v169, 0xffff0000, v159
	v_and_b32_e32 v168, 0xffff0000, v158
	s_waitcnt vmcnt(14)
	v_mov_b32_e32 v157, v220
	v_mov_b32_e32 v158, v221
	v_mov_b32_e32 v159, v222
	v_mov_b32_e32 v146, v191
	v_pk_fma_f32 v[0:1], v[0:1], v[190:191], v[32:33] op_sel_hi:[1,0,1]
	v_pk_fma_f32 v[2:3], v[2:3], v[190:191], v[34:35] op_sel_hi:[1,0,1]
	v_pk_fma_f32 v[4:5], v[4:5], v[190:191], v[36:37] op_sel_hi:[1,0,1]
	v_pk_fma_f32 v[6:7], v[6:7], v[190:191], v[38:39] op_sel_hi:[1,0,1]
	v_pk_fma_f32 v[8:9], v[8:9], v[190:191], v[40:41] op_sel_hi:[1,0,1]
	v_pk_fma_f32 v[10:11], v[10:11], v[190:191], v[42:43] op_sel_hi:[1,0,1]
	v_pk_fma_f32 v[12:13], v[12:13], v[190:191], v[44:45] op_sel_hi:[1,0,1]
	v_pk_fma_f32 v[14:15], v[14:15], v[190:191], v[46:47] op_sel_hi:[1,0,1]
	s_waitcnt vmcnt(12)
	v_mov_b32_e32 v183, v224
	v_mov_b32_e32 v184, v225
	v_mov_b32_e32 v185, v226
	s_waitcnt vmcnt(10)
	v_mov_b32_e32 v189, v228
	v_mov_b32_e32 v190, v229
	v_mov_b32_e32 v191, v230
	s_waitcnt vmcnt(8)
	v_mov_b32_e32 v195, v232
	v_mov_b32_e32 v196, v233
	v_mov_b32_e32 v197, v234
	ds_read2_b32 v[220:221], v177 offset0:32 offset1:36
	ds_read2_b32 v[222:223], v177 offset0:40 offset1:44
	ds_read2_b32 v[242:243], v177 offset0:48 offset1:52
	ds_read2_b32 v[244:245], v177 offset0:56 offset1:60
	v_cvt_scalef32_pk32_f32_fp6 v[96:127], v[154:159], 1.0
	ds_read_u16 v131, v152 offset:128
	ds_read_u16 v135, v152 offset:136
	ds_read_u16 v139, v152 offset:144
	ds_read_u16 v143, v152 offset:152
	ds_read_u16 v153, v152 offset:160
	ds_read_u16 v154, v152 offset:168
	ds_read_u16 v155, v152 offset:176
	ds_read_u16 v152, v152 offset:184
	v_pk_fma_f32 v[144:145], v[16:17], v[146:147], v[0:1] op_sel_hi:[1,0,1]
	v_pk_fma_f32 v[148:149], v[18:19], v[146:147], v[2:3] op_sel_hi:[1,0,1]
	v_pk_fma_f32 v[150:151], v[20:21], v[146:147], v[4:5] op_sel_hi:[1,0,1]
	v_pk_fma_f32 v[202:203], v[22:23], v[146:147], v[6:7] op_sel_hi:[1,0,1]
	v_pk_fma_f32 v[208:209], v[24:25], v[146:147], v[8:9] op_sel_hi:[1,0,1]
	v_pk_fma_f32 v[214:215], v[26:27], v[146:147], v[10:11] op_sel_hi:[1,0,1]
	v_pk_fma_f32 v[236:237], v[28:29], v[146:147], v[12:13] op_sel_hi:[1,0,1]
	v_pk_fma_f32 v[146:147], v[30:31], v[146:147], v[14:15] op_sel_hi:[1,0,1]
	s_waitcnt lgkmcnt(11)
	v_pk_fma_f32 v[96:97], v[96:97], v[220:221], v[144:145] op_sel_hi:[1,0,1]
	v_mov_b32_e32 v144, v221
	v_cvt_scalef32_pk32_f32_fp6 v[64:95], v[180:185], 1.0
	v_pk_fma_f32 v[98:99], v[98:99], v[220:221], v[148:149] op_sel_hi:[1,0,1]
	v_pk_fma_f32 v[100:101], v[100:101], v[220:221], v[150:151] op_sel_hi:[1,0,1]
	v_pk_fma_f32 v[102:103], v[102:103], v[220:221], v[202:203] op_sel_hi:[1,0,1]
	v_pk_fma_f32 v[104:105], v[104:105], v[220:221], v[208:209] op_sel_hi:[1,0,1]
	v_pk_fma_f32 v[106:107], v[106:107], v[220:221], v[214:215] op_sel_hi:[1,0,1]
	v_pk_fma_f32 v[108:109], v[108:109], v[220:221], v[236:237] op_sel_hi:[1,0,1]
	v_pk_fma_f32 v[110:111], v[110:111], v[220:221], v[146:147] op_sel_hi:[1,0,1]
	v_pk_fma_f32 v[96:97], v[112:113], v[144:145], v[96:97] op_sel_hi:[1,0,1]
	s_waitcnt lgkmcnt(7)
	v_add_u32_e32 v112, s21, v131
	v_pk_fma_f32 v[98:99], v[114:115], v[144:145], v[98:99] op_sel_hi:[1,0,1]
	v_pk_fma_f32 v[100:101], v[116:117], v[144:145], v[100:101] op_sel_hi:[1,0,1]
	v_pk_fma_f32 v[102:103], v[118:119], v[144:145], v[102:103] op_sel_hi:[1,0,1]
	v_pk_fma_f32 v[104:105], v[120:121], v[144:145], v[104:105] op_sel_hi:[1,0,1]
	v_pk_fma_f32 v[106:107], v[122:123], v[144:145], v[106:107] op_sel_hi:[1,0,1]
	v_pk_fma_f32 v[108:109], v[124:125], v[144:145], v[108:109] op_sel_hi:[1,0,1]
	v_pk_fma_f32 v[110:111], v[126:127], v[144:145], v[110:111] op_sel_hi:[1,0,1]
	s_waitcnt lgkmcnt(6)
	v_add_u32_e32 v113, s21, v135
	s_waitcnt lgkmcnt(5)
	v_add_u32_e32 v114, s21, v139
	s_waitcnt lgkmcnt(4)
	v_add_u32_e32 v115, s21, v143
	s_waitcnt lgkmcnt(3)
	v_add_u32_e32 v116, s21, v153
	s_waitcnt lgkmcnt(2)
	v_add_u32_e32 v117, s21, v154
	s_waitcnt lgkmcnt(1)
	v_add_u32_e32 v118, s21, v155
	s_waitcnt lgkmcnt(0)
	v_add_u32_e32 v119, s21, v152
	v_pk_fma_f32 v[64:65], v[64:65], v[222:223], v[96:97] op_sel_hi:[1,0,1]
	v_mad_u64_u32 v[96:97], s[30:31], v112, s16, v[160:161]
	v_cvt_scalef32_pk32_f32_fp6 v[32:63], v[186:191], 1.0
	v_cvt_scalef32_pk32_f32_fp6 v[0:31], v[192:197], 1.0
	v_mov_b32_e32 v146, v223
	v_pk_fma_f32 v[66:67], v[66:67], v[222:223], v[98:99] op_sel_hi:[1,0,1]
	v_pk_fma_f32 v[68:69], v[68:69], v[222:223], v[100:101] op_sel_hi:[1,0,1]
	v_pk_fma_f32 v[70:71], v[70:71], v[222:223], v[102:103] op_sel_hi:[1,0,1]
	v_pk_fma_f32 v[72:73], v[72:73], v[222:223], v[104:105] op_sel_hi:[1,0,1]
	v_pk_fma_f32 v[74:75], v[74:75], v[222:223], v[106:107] op_sel_hi:[1,0,1]
	v_pk_fma_f32 v[76:77], v[76:77], v[222:223], v[108:109] op_sel_hi:[1,0,1]
	v_pk_fma_f32 v[78:79], v[78:79], v[222:223], v[110:111] op_sel_hi:[1,0,1]
	v_mad_u64_u32 v[98:99], s[30:31], v113, s16, v[160:161]
	v_mad_u64_u32 v[100:101], s[30:31], v114, s16, v[160:161]
	v_mad_u64_u32 v[102:103], s[30:31], v115, s16, v[160:161]
	v_mad_u64_u32 v[104:105], s[30:31], v116, s16, v[160:161]
	v_mad_u64_u32 v[106:107], s[30:31], v117, s16, v[160:161]
	v_mad_u64_u32 v[108:109], s[30:31], v118, s16, v[160:161]
	v_mad_u64_u32 v[110:111], s[30:31], v119, s16, v[160:161]
	global_load_dwordx3 v[180:182], v96, s[2:3]
	global_load_dwordx3 v[226:228], v98, s[2:3]
	global_load_dwordx3 v[186:188], v100, s[2:3]
	global_load_dwordx3 v[230:232], v102, s[2:3]
	global_load_dwordx3 v[192:194], v104, s[2:3]
	global_load_dwordx3 v[234:236], v106, s[2:3]
	global_load_dwordx3 v[222:224], v108, s[2:3]
	global_load_dwordx3 v[238:240], v110, s[2:3]
	s_waitcnt vmcnt(14)
	v_mov_b32_e32 v201, v128
	v_mov_b32_e32 v202, v129
	v_mov_b32_e32 v203, v130
	s_waitcnt vmcnt(12)
	v_mov_b32_e32 v207, v132
	v_mov_b32_e32 v208, v133
	v_mov_b32_e32 v209, v134
	s_waitcnt vmcnt(10)
	v_mov_b32_e32 v213, v136
	v_mov_b32_e32 v214, v137
	v_mov_b32_e32 v215, v138
	s_waitcnt vmcnt(8)
	v_mov_b32_e32 v219, v140
	v_mov_b32_e32 v220, v141
	v_mov_b32_e32 v221, v142
	v_pk_fma_f32 v[64:65], v[80:81], v[146:147], v[64:65] op_sel_hi:[1,0,1]
	v_pk_fma_f32 v[66:67], v[82:83], v[146:147], v[66:67] op_sel_hi:[1,0,1]
	v_pk_fma_f32 v[68:69], v[84:85], v[146:147], v[68:69] op_sel_hi:[1,0,1]
	v_pk_fma_f32 v[70:71], v[86:87], v[146:147], v[70:71] op_sel_hi:[1,0,1]
	v_pk_fma_f32 v[72:73], v[88:89], v[146:147], v[72:73] op_sel_hi:[1,0,1]
	v_pk_fma_f32 v[74:75], v[90:91], v[146:147], v[74:75] op_sel_hi:[1,0,1]
	v_pk_fma_f32 v[76:77], v[92:93], v[146:147], v[76:77] op_sel_hi:[1,0,1]
	v_pk_fma_f32 v[78:79], v[94:95], v[146:147], v[78:79] op_sel_hi:[1,0,1]
	ds_read2_b32 v[196:197], v177 offset0:64 offset1:68
	v_mov_b32_e32 v184, v243
	ds_read2_b32 v[246:247], v177 offset0:72 offset1:76
	ds_read2_b32 v[248:249], v177 offset0:80 offset1:84
	ds_read2_b32 v[250:251], v177 offset0:88 offset1:92
	v_pk_fma_f32 v[32:33], v[32:33], v[242:243], v[64:65] op_sel_hi:[1,0,1]
	v_pk_fma_f32 v[34:35], v[34:35], v[242:243], v[66:67] op_sel_hi:[1,0,1]
	v_pk_fma_f32 v[36:37], v[36:37], v[242:243], v[68:69] op_sel_hi:[1,0,1]
	v_pk_fma_f32 v[38:39], v[38:39], v[242:243], v[70:71] op_sel_hi:[1,0,1]
	v_pk_fma_f32 v[40:41], v[40:41], v[242:243], v[72:73] op_sel_hi:[1,0,1]
	v_pk_fma_f32 v[42:43], v[42:43], v[242:243], v[74:75] op_sel_hi:[1,0,1]
	v_pk_fma_f32 v[44:45], v[44:45], v[242:243], v[76:77] op_sel_hi:[1,0,1]
	v_pk_fma_f32 v[46:47], v[46:47], v[242:243], v[78:79] op_sel_hi:[1,0,1]
	v_cvt_scalef32_pk32_f32_fp6 v[128:159], v[198:203], 1.0
	v_cvt_scalef32_pk32_f32_fp6 v[96:127], v[204:209], 1.0
	v_cvt_scalef32_pk32_f32_fp6 v[64:95], v[210:215], 1.0
	v_pk_fma_f32 v[198:199], v[48:49], v[184:185], v[32:33] op_sel_hi:[1,0,1]
	v_pk_fma_f32 v[200:201], v[50:51], v[184:185], v[34:35] op_sel_hi:[1,0,1]
	v_pk_fma_f32 v[202:203], v[52:53], v[184:185], v[36:37] op_sel_hi:[1,0,1]
	v_pk_fma_f32 v[204:205], v[54:55], v[184:185], v[38:39] op_sel_hi:[1,0,1]
	v_pk_fma_f32 v[206:207], v[56:57], v[184:185], v[40:41] op_sel_hi:[1,0,1]
	v_pk_fma_f32 v[208:209], v[58:59], v[184:185], v[42:43] op_sel_hi:[1,0,1]
	v_pk_fma_f32 v[210:211], v[60:61], v[184:185], v[44:45] op_sel_hi:[1,0,1]
	v_pk_fma_f32 v[184:185], v[62:63], v[184:185], v[46:47] op_sel_hi:[1,0,1]
	ds_read_u16 v183, v179 offset:16384
	ds_read_u16 v189, v179 offset:16392
	ds_read_u16 v191, v179 offset:16400
	ds_read_u16 v195, v179 offset:16408
	ds_read_u16 v212, v179 offset:16416
	ds_read_u16 v213, v179 offset:16424
	ds_read_u16 v214, v179 offset:16432
	ds_read_u16 v179, v179 offset:16440
	v_mov_b32_e32 v190, v245
	v_pk_fma_f32 v[0:1], v[0:1], v[244:245], v[198:199] op_sel_hi:[1,0,1]
	v_pk_fma_f32 v[2:3], v[2:3], v[244:245], v[200:201] op_sel_hi:[1,0,1]
	v_pk_fma_f32 v[4:5], v[4:5], v[244:245], v[202:203] op_sel_hi:[1,0,1]
	v_pk_fma_f32 v[6:7], v[6:7], v[244:245], v[204:205] op_sel_hi:[1,0,1]
	v_pk_fma_f32 v[8:9], v[8:9], v[244:245], v[206:207] op_sel_hi:[1,0,1]
	v_pk_fma_f32 v[10:11], v[10:11], v[244:245], v[208:209] op_sel_hi:[1,0,1]
	v_pk_fma_f32 v[12:13], v[12:13], v[244:245], v[210:211] op_sel_hi:[1,0,1]
	v_pk_fma_f32 v[14:15], v[14:15], v[244:245], v[184:185] op_sel_hi:[1,0,1]
	s_cselect_b32 s29, s22, s17
	s_waitcnt lgkmcnt(5)
	v_pk_fma_f32 v[0:1], v[16:17], v[190:191], v[0:1] op_sel_hi:[1,0,1]
	v_pk_fma_f32 v[2:3], v[18:19], v[190:191], v[2:3] op_sel_hi:[1,0,1]
	v_pk_fma_f32 v[4:5], v[20:21], v[190:191], v[4:5] op_sel_hi:[1,0,1]
	v_pk_fma_f32 v[6:7], v[22:23], v[190:191], v[6:7] op_sel_hi:[1,0,1]
	v_pk_fma_f32 v[8:9], v[24:25], v[190:191], v[8:9] op_sel_hi:[1,0,1]
	v_pk_fma_f32 v[10:11], v[26:27], v[190:191], v[10:11] op_sel_hi:[1,0,1]
	v_pk_fma_f32 v[12:13], v[28:29], v[190:191], v[12:13] op_sel_hi:[1,0,1]
	v_pk_fma_f32 v[14:15], v[30:31], v[190:191], v[14:15] op_sel_hi:[1,0,1]
	s_lshl_b64 s[14:15], s[12:13], 14
	s_lshl_b32 s13, s29, 14
	v_pk_fma_f32 v[0:1], v[128:129], v[196:197], v[0:1] op_sel_hi:[1,0,1]
	v_pk_fma_f32 v[2:3], v[130:131], v[196:197], v[2:3] op_sel_hi:[1,0,1]
	v_pk_fma_f32 v[4:5], v[132:133], v[196:197], v[4:5] op_sel_hi:[1,0,1]
	v_pk_fma_f32 v[6:7], v[134:135], v[196:197], v[6:7] op_sel_hi:[1,0,1]
	v_pk_fma_f32 v[8:9], v[136:137], v[196:197], v[8:9] op_sel_hi:[1,0,1]
	v_pk_fma_f32 v[10:11], v[138:139], v[196:197], v[10:11] op_sel_hi:[1,0,1]
	v_pk_fma_f32 v[12:13], v[140:141], v[196:197], v[12:13] op_sel_hi:[1,0,1]
	v_pk_fma_f32 v[14:15], v[142:143], v[196:197], v[14:15] op_sel_hi:[1,0,1]
	v_mov_b32_e32 v16, v197
	v_pk_fma_f32 v[0:1], v[144:145], v[16:17], v[0:1] op_sel_hi:[1,0,1]
	v_pk_fma_f32 v[2:3], v[146:147], v[16:17], v[2:3] op_sel_hi:[1,0,1]
	v_pk_fma_f32 v[4:5], v[148:149], v[16:17], v[4:5] op_sel_hi:[1,0,1]
	v_pk_fma_f32 v[6:7], v[150:151], v[16:17], v[6:7] op_sel_hi:[1,0,1]
	v_pk_fma_f32 v[8:9], v[152:153], v[16:17], v[8:9] op_sel_hi:[1,0,1]
	v_pk_fma_f32 v[10:11], v[154:155], v[16:17], v[10:11] op_sel_hi:[1,0,1]
	v_pk_fma_f32 v[12:13], v[156:157], v[16:17], v[12:13] op_sel_hi:[1,0,1]
	v_pk_fma_f32 v[14:15], v[158:159], v[16:17], v[14:15] op_sel_hi:[1,0,1]
	v_add_u32_e32 v16, s13, v183
	v_add_u32_e32 v19, s13, v189
	v_add_u32_e32 v21, s13, v191
	s_waitcnt lgkmcnt(4)
	v_add_u32_e32 v23, s13, v195
	s_waitcnt lgkmcnt(3)
	v_add_u32_e32 v30, s13, v212
	s_waitcnt lgkmcnt(2)
	v_add_u32_e32 v128, s13, v213
	s_waitcnt lgkmcnt(1)
	v_add_u32_e32 v129, s13, v214
	s_waitcnt lgkmcnt(0)
	v_add_u32_e32 v130, s13, v179
	v_mad_u64_u32 v[16:17], s[30:31], v16, s16, v[160:161]
	v_pk_fma_f32 v[0:1], v[96:97], v[246:247], v[0:1] op_sel_hi:[1,0,1]
	v_pk_fma_f32 v[2:3], v[98:99], v[246:247], v[2:3] op_sel_hi:[1,0,1]
	v_pk_fma_f32 v[4:5], v[100:101], v[246:247], v[4:5] op_sel_hi:[1,0,1]
	v_mad_u64_u32 v[24:25], s[30:31], v19, s16, v[160:161]
	v_mad_u64_u32 v[26:27], s[30:31], v21, s16, v[160:161]
	v_mad_u64_u32 v[28:29], s[30:31], v23, s16, v[160:161]
	v_mad_u64_u32 v[30:31], s[30:31], v30, s16, v[160:161]
	v_mad_u64_u32 v[96:97], s[30:31], v128, s16, v[160:161]
	v_mad_u64_u32 v[98:99], s[30:31], v129, s16, v[160:161]
	v_mad_u64_u32 v[100:101], s[30:31], v130, s16, v[160:161]
	global_load_dwordx3 v[134:136], v16, s[2:3]
	global_load_dwordx3 v[152:154], v24, s[2:3]
	global_load_dwordx3 v[128:130], v26, s[2:3]
	global_load_dwordx3 v[156:158], v28, s[2:3]
	global_load_dwordx3 v[140:142], v30, s[2:3]
	global_load_dwordx3 v[198:200], v96, s[2:3]
	global_load_dwordx3 v[146:148], v98, s[2:3]
	global_load_dwordx3 v[202:204], v100, s[2:3]
	v_mov_b32_e32 v18, v247
	v_pk_fma_f32 v[6:7], v[102:103], v[246:247], v[6:7] op_sel_hi:[1,0,1]
	v_pk_fma_f32 v[8:9], v[104:105], v[246:247], v[8:9] op_sel_hi:[1,0,1]
	v_pk_fma_f32 v[10:11], v[106:107], v[246:247], v[10:11] op_sel_hi:[1,0,1]
	v_pk_fma_f32 v[12:13], v[108:109], v[246:247], v[12:13] op_sel_hi:[1,0,1]
	v_pk_fma_f32 v[14:15], v[110:111], v[246:247], v[14:15] op_sel_hi:[1,0,1]
	s_waitcnt vmcnt(14)
	v_mov_b32_e32 v183, v226
	v_mov_b32_e32 v184, v227
	v_mov_b32_e32 v185, v228
	v_pk_fma_f32 v[0:1], v[112:113], v[18:19], v[0:1] op_sel_hi:[1,0,1]
	v_pk_fma_f32 v[2:3], v[114:115], v[18:19], v[2:3] op_sel_hi:[1,0,1]
	v_pk_fma_f32 v[4:5], v[116:117], v[18:19], v[4:5] op_sel_hi:[1,0,1]
	v_pk_fma_f32 v[6:7], v[118:119], v[18:19], v[6:7] op_sel_hi:[1,0,1]
	v_pk_fma_f32 v[8:9], v[120:121], v[18:19], v[8:9] op_sel_hi:[1,0,1]
	v_pk_fma_f32 v[10:11], v[122:123], v[18:19], v[10:11] op_sel_hi:[1,0,1]
	v_pk_fma_f32 v[12:13], v[124:125], v[18:19], v[12:13] op_sel_hi:[1,0,1]
	v_pk_fma_f32 v[14:15], v[126:127], v[18:19], v[14:15] op_sel_hi:[1,0,1]
	ds_read2_b32 v[214:215], v177 offset0:96 offset1:100
	v_mov_b32_e32 v20, v249
	v_pk_fma_f32 v[0:1], v[64:65], v[248:249], v[0:1] op_sel_hi:[1,0,1]
	v_pk_fma_f32 v[2:3], v[66:67], v[248:249], v[2:3] op_sel_hi:[1,0,1]
	v_pk_fma_f32 v[4:5], v[68:69], v[248:249], v[4:5] op_sel_hi:[1,0,1]
	v_pk_fma_f32 v[6:7], v[70:71], v[248:249], v[6:7] op_sel_hi:[1,0,1]
	v_pk_fma_f32 v[8:9], v[72:73], v[248:249], v[8:9] op_sel_hi:[1,0,1]
	v_pk_fma_f32 v[10:11], v[74:75], v[248:249], v[10:11] op_sel_hi:[1,0,1]
	v_pk_fma_f32 v[12:13], v[76:77], v[248:249], v[12:13] op_sel_hi:[1,0,1]
	v_pk_fma_f32 v[14:15], v[78:79], v[248:249], v[14:15] op_sel_hi:[1,0,1]
	s_waitcnt vmcnt(12)
	v_mov_b32_e32 v189, v230
	v_mov_b32_e32 v190, v231
	v_mov_b32_e32 v191, v232
	v_cvt_scalef32_pk32_f32_fp6 v[32:63], v[216:221], 1.0
	v_pk_fma_f32 v[0:1], v[80:81], v[20:21], v[0:1] op_sel_hi:[1,0,1]
	v_pk_fma_f32 v[2:3], v[82:83], v[20:21], v[2:3] op_sel_hi:[1,0,1]
	v_pk_fma_f32 v[4:5], v[84:85], v[20:21], v[4:5] op_sel_hi:[1,0,1]
	v_pk_fma_f32 v[6:7], v[86:87], v[20:21], v[6:7] op_sel_hi:[1,0,1]
	v_pk_fma_f32 v[8:9], v[88:89], v[20:21], v[8:9] op_sel_hi:[1,0,1]
	v_pk_fma_f32 v[10:11], v[90:91], v[20:21], v[10:11] op_sel_hi:[1,0,1]
	v_pk_fma_f32 v[12:13], v[92:93], v[20:21], v[12:13] op_sel_hi:[1,0,1]
	v_pk_fma_f32 v[14:15], v[94:95], v[20:21], v[14:15] op_sel_hi:[1,0,1]
	ds_read2_b32 v[216:217], v177 offset0:104 offset1:108
	v_mov_b32_e32 v22, v251
	v_pk_fma_f32 v[0:1], v[32:33], v[250:251], v[0:1] op_sel_hi:[1,0,1]
	v_pk_fma_f32 v[2:3], v[34:35], v[250:251], v[2:3] op_sel_hi:[1,0,1]
	v_pk_fma_f32 v[4:5], v[36:37], v[250:251], v[4:5] op_sel_hi:[1,0,1]
	v_pk_fma_f32 v[6:7], v[38:39], v[250:251], v[6:7] op_sel_hi:[1,0,1]
	v_pk_fma_f32 v[8:9], v[40:41], v[250:251], v[8:9] op_sel_hi:[1,0,1]
	v_pk_fma_f32 v[10:11], v[42:43], v[250:251], v[10:11] op_sel_hi:[1,0,1]
	v_pk_fma_f32 v[12:13], v[44:45], v[250:251], v[12:13] op_sel_hi:[1,0,1]
	v_pk_fma_f32 v[14:15], v[46:47], v[250:251], v[14:15] op_sel_hi:[1,0,1]
	s_waitcnt vmcnt(10)
	v_mov_b32_e32 v195, v234
	v_mov_b32_e32 v196, v235
	v_mov_b32_e32 v197, v236
	v_mov_b32_e32 v162, v176
	v_pk_fma_f32 v[132:133], v[48:49], v[22:23], v[0:1] op_sel_hi:[1,0,1]
	v_pk_fma_f32 v[138:139], v[50:51], v[22:23], v[2:3] op_sel_hi:[1,0,1]
	v_pk_fma_f32 v[144:145], v[52:53], v[22:23], v[4:5] op_sel_hi:[1,0,1]
	v_pk_fma_f32 v[150:151], v[54:55], v[22:23], v[6:7] op_sel_hi:[1,0,1]
	v_pk_fma_f32 v[206:207], v[56:57], v[22:23], v[8:9] op_sel_hi:[1,0,1]
	v_pk_fma_f32 v[208:209], v[58:59], v[22:23], v[10:11] op_sel_hi:[1,0,1]
	v_pk_fma_f32 v[210:211], v[60:61], v[22:23], v[12:13] op_sel_hi:[1,0,1]
	v_pk_fma_f32 v[212:213], v[62:63], v[22:23], v[14:15] op_sel_hi:[1,0,1]
	s_waitcnt vmcnt(8)
	v_mov_b32_e32 v225, v238
	v_mov_b32_e32 v226, v239
	v_mov_b32_e32 v227, v240
	ds_read2_b32 v[218:219], v177 offset0:112 offset1:116
	v_cvt_scalef32_pk32_f32_fp6 v[96:127], v[180:185], 1.0
	s_add_u32 s14, s26, s14
	ds_read2_b32 v[220:221], v177 offset0:120 offset1:124
	s_waitcnt lgkmcnt(3)
	v_pk_fma_f32 v[96:97], v[96:97], v[214:215], v[132:133] op_sel_hi:[1,0,1]
	v_pk_fma_f32 v[98:99], v[98:99], v[214:215], v[138:139] op_sel_hi:[1,0,1]
	v_pk_fma_f32 v[100:101], v[100:101], v[214:215], v[144:145] op_sel_hi:[1,0,1]
	v_pk_fma_f32 v[102:103], v[102:103], v[214:215], v[150:151] op_sel_hi:[1,0,1]
	v_pk_fma_f32 v[104:105], v[104:105], v[214:215], v[206:207] op_sel_hi:[1,0,1]
	v_pk_fma_f32 v[106:107], v[106:107], v[214:215], v[208:209] op_sel_hi:[1,0,1]
	v_pk_fma_f32 v[108:109], v[108:109], v[214:215], v[210:211] op_sel_hi:[1,0,1]
	v_pk_fma_f32 v[110:111], v[110:111], v[214:215], v[212:213] op_sel_hi:[1,0,1]
	v_mov_b32_e32 v132, v215
	s_addc_u32 s15, s27, s15
	v_cvt_scalef32_pk32_f32_fp6 v[64:95], v[186:191], 1.0
	v_add_u32_e32 v162, s18, v162
	v_pk_fma_f32 v[96:97], v[112:113], v[132:133], v[96:97] op_sel_hi:[1,0,1]
	v_pk_fma_f32 v[98:99], v[114:115], v[132:133], v[98:99] op_sel_hi:[1,0,1]
	v_pk_fma_f32 v[100:101], v[116:117], v[132:133], v[100:101] op_sel_hi:[1,0,1]
	v_pk_fma_f32 v[102:103], v[118:119], v[132:133], v[102:103] op_sel_hi:[1,0,1]
	v_pk_fma_f32 v[104:105], v[120:121], v[132:133], v[104:105] op_sel_hi:[1,0,1]
	v_pk_fma_f32 v[106:107], v[122:123], v[132:133], v[106:107] op_sel_hi:[1,0,1]
	v_pk_fma_f32 v[108:109], v[124:125], v[132:133], v[108:109] op_sel_hi:[1,0,1]
	v_pk_fma_f32 v[110:111], v[126:127], v[132:133], v[110:111] op_sel_hi:[1,0,1]
	v_lshl_add_u64 v[180:181], v[162:163], 2, s[14:15]
	s_waitcnt lgkmcnt(2)
	v_mov_b32_e32 v162, v217
	v_pk_fma_f32 v[64:65], v[64:65], v[216:217], v[96:97] op_sel_hi:[1,0,1]
	v_pk_fma_f32 v[66:67], v[66:67], v[216:217], v[98:99] op_sel_hi:[1,0,1]
	v_pk_fma_f32 v[68:69], v[68:69], v[216:217], v[100:101] op_sel_hi:[1,0,1]
	v_pk_fma_f32 v[70:71], v[70:71], v[216:217], v[102:103] op_sel_hi:[1,0,1]
	v_pk_fma_f32 v[72:73], v[72:73], v[216:217], v[104:105] op_sel_hi:[1,0,1]
	v_pk_fma_f32 v[74:75], v[74:75], v[216:217], v[106:107] op_sel_hi:[1,0,1]
	v_pk_fma_f32 v[76:77], v[76:77], v[216:217], v[108:109] op_sel_hi:[1,0,1]
	v_pk_fma_f32 v[78:79], v[78:79], v[216:217], v[110:111] op_sel_hi:[1,0,1]
	v_cvt_scalef32_pk32_f32_fp6 v[32:63], v[192:197], 1.0
	v_pk_fma_f32 v[64:65], v[80:81], v[162:163], v[64:65] op_sel_hi:[1,0,1]
	v_pk_fma_f32 v[66:67], v[82:83], v[162:163], v[66:67] op_sel_hi:[1,0,1]
	v_pk_fma_f32 v[68:69], v[84:85], v[162:163], v[68:69] op_sel_hi:[1,0,1]
	v_pk_fma_f32 v[70:71], v[86:87], v[162:163], v[70:71] op_sel_hi:[1,0,1]
	v_pk_fma_f32 v[72:73], v[88:89], v[162:163], v[72:73] op_sel_hi:[1,0,1]
	v_pk_fma_f32 v[74:75], v[90:91], v[162:163], v[74:75] op_sel_hi:[1,0,1]
	v_pk_fma_f32 v[76:77], v[92:93], v[162:163], v[76:77] op_sel_hi:[1,0,1]
	v_pk_fma_f32 v[78:79], v[94:95], v[162:163], v[78:79] op_sel_hi:[1,0,1]
	s_waitcnt lgkmcnt(1)
	v_mov_b32_e32 v182, v219
	v_pk_fma_f32 v[32:33], v[32:33], v[218:219], v[64:65] op_sel_hi:[1,0,1]
	v_pk_fma_f32 v[34:35], v[34:35], v[218:219], v[66:67] op_sel_hi:[1,0,1]
	v_pk_fma_f32 v[36:37], v[36:37], v[218:219], v[68:69] op_sel_hi:[1,0,1]
	v_pk_fma_f32 v[38:39], v[38:39], v[218:219], v[70:71] op_sel_hi:[1,0,1]
	v_pk_fma_f32 v[40:41], v[40:41], v[218:219], v[72:73] op_sel_hi:[1,0,1]
	v_pk_fma_f32 v[42:43], v[42:43], v[218:219], v[74:75] op_sel_hi:[1,0,1]
	v_pk_fma_f32 v[44:45], v[44:45], v[218:219], v[76:77] op_sel_hi:[1,0,1]
	v_pk_fma_f32 v[46:47], v[46:47], v[218:219], v[78:79] op_sel_hi:[1,0,1]
	v_cvt_scalef32_pk32_f32_fp6 v[0:31], v[222:227], 1.0
	v_pk_fma_f32 v[32:33], v[48:49], v[182:183], v[32:33] op_sel_hi:[1,0,1]
	v_pk_fma_f32 v[34:35], v[50:51], v[182:183], v[34:35] op_sel_hi:[1,0,1]
	v_pk_fma_f32 v[36:37], v[52:53], v[182:183], v[36:37] op_sel_hi:[1,0,1]
	v_pk_fma_f32 v[38:39], v[54:55], v[182:183], v[38:39] op_sel_hi:[1,0,1]
	v_pk_fma_f32 v[40:41], v[56:57], v[182:183], v[40:41] op_sel_hi:[1,0,1]
	v_pk_fma_f32 v[42:43], v[58:59], v[182:183], v[42:43] op_sel_hi:[1,0,1]
	v_pk_fma_f32 v[44:45], v[60:61], v[182:183], v[44:45] op_sel_hi:[1,0,1]
	v_pk_fma_f32 v[46:47], v[62:63], v[182:183], v[46:47] op_sel_hi:[1,0,1]
	s_waitcnt lgkmcnt(0)
; __device__ __forceinline__ int fresh_lane() { int l; asm volatile("v_mbcnt_lo_u32_b32 %0, -1, 0\n\tv_mbcnt_hi_u32_b32 %0, -1, %0" : "=v"(l)); return l; }
; __device__ __forceinline__ float bflo(unsigned w) { return __uint_as_float(w << 16); }
; __device__ __forceinline__ float bfhi(unsigned w) { return __uint_as_float(w & 0xffff0000u); }
; __device__ __forceinline__ float wave_sum(float v) { v = dpp_add16(v); return (rdlane(v, 0) + rdlane(v, 16)) + (rdlane(v, 32) + rdlane(v, 48)); }
; __device__ __forceinline__ void p12_peer(Frame& F) {
;     ...
;               float r8[8], r4[4];
; #pragma unroll
;               for (int m = 0; m < 8; ++m) { const float lo_v = (m & 1) ? acc2[m >> 1].y : acc2[m >> 1].x, hi_v = (m & 1) ? acc2[4 + (m >> 1)].y : acc2[4 + (m >> 1)].x;
;                   const float keep = hi5 ? hi_v : lo_v, send = hi5 ? lo_v : hi_v;
;                   r8[m] = keep + __builtin_bit_cast(float, __builtin_amdgcn_ds_bpermute((F.lane ^ 32) << 2, __builtin_bit_cast(int, send))); }
; #pragma unroll
;               for (int m = 0; m < 4; ++m) { const float keep = hi4 ? r8[4 + m] : r8[m], send = hi4 ? r8[m] : r8[4 + m];
;                   r4[m] = keep + __builtin_bit_cast(float, __builtin_amdgcn_ds_bpermute((F.lane ^ 16) << 2, __builtin_bit_cast(int, send))); }
;               int lo3_ = lo_; asm volatile("" : "+v"(lo3_));
;               const size_t col = (size_t)t * D_ + (size_t)(unsigned)(256 * c + lo3_);
;               const f32x4 o = {r4[0] + bflo(hb.x), r4[1] + bfhi(hb.x), r4[2] + bflo(hb.y), r4[3] + bfhi(hb.y)};
;               SSQ[i * 64 + F.lane] += (o.x * o.x + o.y * o.y) + (o.z * o.z + o.w * o.w);
;               *(f32x4*)(F.out + col) = o;
;           }
;       }
;     ...
;       __builtin_amdgcn_fence(__ATOMIC_SEQ_CST, "agent");
;       const int l2_ = fresh_lane(), lo2_ = 16 * (l2_ & 15) + 4 * (l2_ >> 4);
; #pragma unroll
;       for (int i = 0; i < 4; ++i) { const int t = F.gw + i * F.NGW;
;           const float rs = 1.0f / sqrtf(wave_sum(SSQ[i * 64 + l2_]) * (1.f / D_) + 1e-6f);
; _Pragma("nounroll")
;           for (int c0 = 0; c0 < 16; c0 += 8) {
; #pragma unroll
;               for (int c = c0; c < c0 + 8; ++c) { const size_t col = (size_t)t * D_ + (size_t)(unsigned)(256 * c + lo2_); const f32x4 gn = *(const f32x4*)(lnf + (256 * c + lo2_));
	v_mov_b32_e32 v184, v221
	v_pk_fma_f32 v[0:1], v[0:1], v[220:221], v[32:33] op_sel_hi:[1,0,1]
	v_pk_fma_f32 v[2:3], v[2:3], v[220:221], v[34:35] op_sel_hi:[1,0,1]
	v_pk_fma_f32 v[4:5], v[4:5], v[220:221], v[36:37] op_sel_hi:[1,0,1]
	v_pk_fma_f32 v[6:7], v[6:7], v[220:221], v[38:39] op_sel_hi:[1,0,1]
	v_pk_fma_f32 v[8:9], v[8:9], v[220:221], v[40:41] op_sel_hi:[1,0,1]
	v_pk_fma_f32 v[10:11], v[10:11], v[220:221], v[42:43] op_sel_hi:[1,0,1]
	v_pk_fma_f32 v[12:13], v[12:13], v[220:221], v[44:45] op_sel_hi:[1,0,1]
	v_pk_fma_f32 v[14:15], v[14:15], v[220:221], v[46:47] op_sel_hi:[1,0,1]
	v_pk_fma_f32 v[0:1], v[16:17], v[184:185], v[0:1] op_sel_hi:[1,0,1]
	v_pk_fma_f32 v[2:3], v[18:19], v[184:185], v[2:3] op_sel_hi:[1,0,1]
	v_pk_fma_f32 v[4:5], v[20:21], v[184:185], v[4:5] op_sel_hi:[1,0,1]
	v_pk_fma_f32 v[6:7], v[22:23], v[184:185], v[6:7] op_sel_hi:[1,0,1]
	v_pk_fma_f32 v[8:9], v[24:25], v[184:185], v[8:9] op_sel_hi:[1,0,1]
	v_pk_fma_f32 v[10:11], v[26:27], v[184:185], v[10:11] op_sel_hi:[1,0,1]
	v_pk_fma_f32 v[12:13], v[28:29], v[184:185], v[12:13] op_sel_hi:[1,0,1]
	v_pk_fma_f32 v[14:15], v[30:31], v[184:185], v[14:15] op_sel_hi:[1,0,1]
	v_cndmask_b32_e32 v18, v0, v8, vcc
	v_cndmask_b32_e32 v19, v1, v9, vcc
	v_cndmask_b32_e32 v20, v2, v10, vcc
	v_cndmask_b32_e32 v21, v3, v11, vcc
	v_cndmask_b32_e32 v22, v4, v12, vcc
	v_cndmask_b32_e32 v23, v5, v13, vcc
	v_cndmask_b32_e32 v24, v6, v14, vcc
	v_cndmask_b32_e32 v25, v7, v15, vcc
	v_cndmask_b32_e32 v17, v10, v2, vcc
	v_cndmask_b32_e32 v16, v8, v0, vcc
	v_cndmask_b32_e32 v3, v11, v3, vcc
	v_cndmask_b32_e32 v2, v9, v1, vcc
	v_cndmask_b32_e32 v1, v14, v6, vcc
	v_cndmask_b32_e32 v0, v12, v4, vcc
	v_cndmask_b32_e32 v6, v13, v5, vcc
	ds_bpermute_b32 v4, v171, v18
	ds_bpermute_b32 v8, v171, v19
	ds_bpermute_b32 v5, v171, v20
	ds_bpermute_b32 v9, v171, v21
	ds_bpermute_b32 v10, v171, v22
	ds_bpermute_b32 v12, v171, v23
	ds_bpermute_b32 v11, v171, v24
	ds_bpermute_b32 v13, v171, v25
	v_cndmask_b32_e32 v7, v15, v7, vcc
	s_waitcnt lgkmcnt(5)
	v_pk_add_f32 v[4:5], v[16:17], v[4:5]
	s_waitcnt lgkmcnt(4)
	v_pk_add_f32 v[2:3], v[2:3], v[8:9]
	s_waitcnt lgkmcnt(1)
	v_pk_add_f32 v[0:1], v[0:1], v[10:11]
	s_waitcnt lgkmcnt(0)
	v_pk_add_f32 v[6:7], v[6:7], v[12:13]
	v_cndmask_b32_e64 v10, v4, v0, s[0:1]
	v_cndmask_b32_e64 v11, v2, v6, s[0:1]
	v_cndmask_b32_e64 v9, v1, v5, s[0:1]
	v_cndmask_b32_e64 v8, v0, v4, s[0:1]
	v_cndmask_b32_e64 v5, v5, v1, s[0:1]
	v_cndmask_b32_e64 v0, v6, v2, s[0:1]
	v_cndmask_b32_e64 v6, v3, v7, s[0:1]
	v_cndmask_b32_e64 v1, v7, v3, s[0:1]
	ds_bpermute_b32 v2, v170, v10
	ds_bpermute_b32 v4, v170, v11
	ds_bpermute_b32 v3, v170, v5
	ds_bpermute_b32 v5, v170, v6
	v_add_u32_e32 v178, s28, v174
	ds_read_b32 v155, v178
	s_addk_i32 s28, 0x100
	s_waitcnt lgkmcnt(2)
	v_pk_add_f32 v[2:3], v[8:9], v[2:3]
	s_waitcnt lgkmcnt(1)
	v_pk_add_f32 v[0:1], v[0:1], v[4:5]
	v_pk_add_f32 v[4:5], v[2:3], v[166:167]
	v_pk_add_f32 v[2:3], v[0:1], v[168:169]
	v_mov_b32_e32 v0, v4
	v_pk_mul_f32 v[6:7], v[2:3], v[2:3]
	v_mov_b32_e32 v1, v2
	v_mov_b32_e32 v2, v5
	v_pk_fma_f32 v[4:5], v[4:5], v[4:5], v[6:7]
	s_addk_i32 s23, 0x80
	s_add_i32 s12, s12, s34
	global_store_dwordx4 v[180:181], v[0:3], off
	s_cmpk_eq_i32 s28, 0x400
	v_add_u32_e32 v177, 0x200, v177
	v_add_f32_e32 v0, v4, v5
	s_waitcnt vmcnt(1)
	v_mov_b32_e32 v149, v202
	v_mov_b32_e32 v150, v203
	v_mov_b32_e32 v151, v204
	v_mov_b32_e32 v143, v198
	v_mov_b32_e32 v144, v199
	v_mov_b32_e32 v145, v200
	v_mov_b32_e32 v131, v156
	v_mov_b32_e32 v132, v157
	v_mov_b32_e32 v133, v158
	v_mov_b32_e32 v137, v152
	v_mov_b32_e32 v138, v153
	v_mov_b32_e32 v139, v154
	s_waitcnt lgkmcnt(0)
	v_add_f32_e32 v0, v155, v0
	ds_write_b32 v178, v0
	s_cbranch_scc0 .LBB0_3403
	s_cmp_eq_u32 s19, 16
	s_mov_b32 s17, s19
	s_cbranch_scc0 .LBB0_3402
	s_waitcnt vmcnt(0) lgkmcnt(0)
	buffer_inv sc1
	v_mbcnt_lo_u32_b32 v0, -1, 0
	v_mbcnt_hi_u32_b32 v0, -1, v0
	v_lshl_add_u32 v7, v0, 2, s20
	v_and_b32_e32 v2, 15, v0
	v_lshrrev_b32_e32 v3, 4, v0
	v_lshlrev_b32_e32 v2, 6, v2
	v_lshl_add_u32 v6, v3, 4, v2
	v_add_u32_e32 v10, 0x1000, v6
	v_add_u32_e32 v11, 0x2000, v6
	v_add_u32_e32 v12, 0x3000, v6
	s_lshl_b64 s[0:1], s[94:95], 14
	s_add_u32 s12, s26, s0
	s_addc_u32 s13, s27, s1
	s_lshl_b64 s[0:1], s[4:5], 14
	s_add_u32 s14, s26, s0
	s_addc_u32 s15, s27, s1
	s_lshl_b64 s[0:1], s[8:9], 14
	s_add_u32 s16, s26, s0
	s_addc_u32 s17, s27, s1
	s_lshl_b64 s[0:1], s[10:11], 14
	s_add_u32 s18, s26, s0
	s_addc_u32 s19, s27, s1
	global_load_dwordx4 v[60:63], v6, s[24:25] offset:0
	global_load_dwordx4 v[64:67], v6, s[24:25] offset:1024
	global_load_dwordx4 v[68:71], v6, s[24:25] offset:2048
	global_load_dwordx4 v[72:75], v6, s[24:25] offset:3072
	global_load_dwordx4 v[76:79], v10, s[24:25] offset:0
	global_load_dwordx4 v[80:83], v10, s[24:25] offset:1024
	global_load_dwordx4 v[84:87], v10, s[24:25] offset:2048
	global_load_dwordx4 v[88:91], v10, s[24:25] offset:3072
	global_load_dwordx4 v[92:95], v11, s[24:25] offset:0
	global_load_dwordx4 v[96:99], v11, s[24:25] offset:1024
	global_load_dwordx4 v[100:103], v11, s[24:25] offset:2048
	global_load_dwordx4 v[104:107], v11, s[24:25] offset:3072
	global_load_dwordx4 v[108:111], v12, s[24:25] offset:0
	global_load_dwordx4 v[112:115], v12, s[24:25] offset:1024
	global_load_dwordx4 v[116:119], v12, s[24:25] offset:2048
	global_load_dwordx4 v[120:123], v12, s[24:25] offset:3072
	global_load_dwordx4 v[124:127], v6, s[12:13] offset:0
	global_load_dwordx4 v[128:131], v6, s[12:13] offset:1024
	global_load_dwordx4 v[132:135], v6, s[12:13] offset:2048
	global_load_dwordx4 v[136:139], v6, s[12:13] offset:3072
	global_load_dwordx4 v[140:143], v10, s[12:13] offset:0
; __device__ __forceinline__ float rdlane(float v, int l) { return __builtin_bit_cast(float, __builtin_amdgcn_readlane(__builtin_bit_cast(int, v), l)); }
; __device__ __forceinline__ float wave_sum(float v) { v = dpp_add16(v); return (rdlane(v, 0) + rdlane(v, 16)) + (rdlane(v, 32) + rdlane(v, 48)); }
; __device__ __forceinline__ void p12_peer(Frame& F) {
;     ...
;       for (int i = 0; i < 4; ++i) { const int t = F.gw + i * F.NGW;
;           const float rs = 1.0f / sqrtf(wave_sum(SSQ[i * 64 + l2_]) * (1.f / D_) + 1e-6f);
; _Pragma("nounroll")
;           for (int c0 = 0; c0 < 16; c0 += 8) {
; #pragma unroll
;               for (int c = c0; c < c0 + 8; ++c) { const size_t col = (size_t)t * D_ + (size_t)(unsigned)(256 * c + lo2_); const f32x4 gn = *(const f32x4*)(lnf + (256 * c + lo2_));
;                   const f32x4 o = *(const f32x4*)(F.out + col);
;                   *(f32x4*)(F.out + col) = (f32x4){o.x * rs * gn.x, o.y * rs * gn.y, o.z * rs * gn.z, o.w * rs * gn.w}; }
	global_load_dwordx4 v[144:147], v10, s[12:13] offset:1024
	global_load_dwordx4 v[148:151], v10, s[12:13] offset:2048
	global_load_dwordx4 v[152:155], v10, s[12:13] offset:3072
	global_load_dwordx4 v[156:159], v11, s[12:13] offset:0
	global_load_dwordx4 v[160:163], v11, s[12:13] offset:1024
	global_load_dwordx4 v[164:167], v11, s[12:13] offset:2048
	global_load_dwordx4 v[168:171], v11, s[12:13] offset:3072
	global_load_dwordx4 v[172:175], v12, s[12:13] offset:0
	global_load_dwordx4 v[176:179], v12, s[12:13] offset:1024
	global_load_dwordx4 v[180:183], v12, s[12:13] offset:2048
	global_load_dwordx4 v[184:187], v12, s[12:13] offset:3072
	global_load_dwordx4 v[188:191], v6, s[14:15] offset:0
	global_load_dwordx4 v[192:195], v6, s[14:15] offset:1024
	global_load_dwordx4 v[196:199], v6, s[14:15] offset:2048
	global_load_dwordx4 v[200:203], v6, s[14:15] offset:3072
	global_load_dwordx4 v[204:207], v10, s[14:15] offset:0
	global_load_dwordx4 v[208:211], v10, s[14:15] offset:1024
	global_load_dwordx4 v[212:215], v10, s[14:15] offset:2048
	global_load_dwordx4 v[216:219], v10, s[14:15] offset:3072
	global_load_dwordx4 v[220:223], v11, s[14:15] offset:0
	global_load_dwordx4 v[224:227], v11, s[14:15] offset:1024
	global_load_dwordx4 v[228:231], v11, s[14:15] offset:2048
	global_load_dwordx4 v[232:235], v11, s[14:15] offset:3072
	global_load_dwordx4 v[236:239], v12, s[14:15] offset:0
	global_load_dwordx4 v[240:243], v12, s[14:15] offset:1024
	global_load_dwordx4 v[244:247], v12, s[14:15] offset:2048
	global_load_dwordx4 v[248:251], v12, s[14:15] offset:3072
	ds_read_b32 v1, v7 offset:4096
	s_waitcnt lgkmcnt(0)
	v_add_f32_dpp v1, v1, v1 quad_perm:[1,0,3,2] row_mask:0xf bank_mask:0xf bound_ctrl:1
	s_nop 1
	v_add_f32_dpp v1, v1, v1 quad_perm:[2,3,0,1] row_mask:0xf bank_mask:0xf bound_ctrl:1
	s_nop 1
	v_add_f32_dpp v1, v1, v1 row_half_mirror row_mask:0xf bank_mask:0xf bound_ctrl:1
	s_nop 1
	v_add_f32_dpp v1, v1, v1 row_mirror row_mask:0xf bank_mask:0xf bound_ctrl:1
	s_nop 0
	v_readlane_b32 s1, v1, 16
	v_readlane_b32 s0, v1, 0
	s_nop 0
	v_mov_b32_e32 v3, s1
	v_readlane_b32 s1, v1, 48
	v_add_f32_e32 v3, s0, v3
	v_readlane_b32 s0, v1, 32
	v_mov_b32_e32 v1, s1
	s_nop 0
	v_add_f32_e32 v1, s0, v1
	v_add_f32_e32 v1, v3, v1
	v_mov_b32_e32 v3, 0x358637bd
	v_fmac_f32_e32 v3, 0x39800000, v1
	s_mov_b32 s0, 0xf800000
	v_mul_f32_e32 v1, 0x4f800000, v3
	v_cmp_gt_f32_e32 vcc, s0, v3
	s_nop 1
	v_cndmask_b32_e32 v1, v3, v1, vcc
	v_sqrt_f32_e32 v3, v1
	s_nop 0
	v_add_u32_e32 v4, -1, v3
	v_fma_f32 v5, -v4, v3, v1
	v_cmp_ge_f32_e64 s[0:1], 0, v5
	v_add_u32_e32 v5, 1, v3
	s_nop 0
	v_cndmask_b32_e64 v4, v3, v4, s[0:1]
	v_fma_f32 v3, -v5, v3, v1
	v_cmp_lt_f32_e64 s[0:1], 0, v3
	s_nop 1
	v_cndmask_b32_e64 v3, v4, v5, s[0:1]
	v_mul_f32_e32 v4, 0x37800000, v3
	v_cndmask_b32_e32 v3, v3, v4, vcc
	v_mov_b32_e32 v4, 0x260
	v_cmp_class_f32_e32 vcc, v1, v4
	s_nop 1
	v_cndmask_b32_e32 v3, v3, v1, vcc
	v_div_scale_f32 v4, s[0:1], v3, v3, 1.0
	v_rcp_f32_e32 v5, v4
	s_nop 0
	v_fma_f32 v0, -v4, v5, 1.0
	v_fmac_f32_e32 v5, v0, v5
	v_div_scale_f32 v0, vcc, 1.0, v3, 1.0
	v_mul_f32_e32 v2, v0, v5
	v_fma_f32 v8, -v4, v2, v0
	v_fmac_f32_e32 v2, v8, v5
	v_fma_f32 v0, -v4, v2, v0
	v_div_fmas_f32 v0, v0, v5, v2
	v_div_fixup_f32 v2, v0, v3, 1.0
	v_mov_b32_e32 v40, v2
	v_mov_b32_e32 v41, v2
	ds_read_b32 v1, v7 offset:4352
	s_waitcnt lgkmcnt(0)
	v_add_f32_dpp v1, v1, v1 quad_perm:[1,0,3,2] row_mask:0xf bank_mask:0xf bound_ctrl:1
	s_nop 1
	v_add_f32_dpp v1, v1, v1 quad_perm:[2,3,0,1] row_mask:0xf bank_mask:0xf bound_ctrl:1
	s_nop 1
	v_add_f32_dpp v1, v1, v1 row_half_mirror row_mask:0xf bank_mask:0xf bound_ctrl:1
	s_nop 1
	v_add_f32_dpp v1, v1, v1 row_mirror row_mask:0xf bank_mask:0xf bound_ctrl:1
	s_nop 0
	v_readlane_b32 s1, v1, 16
	v_readlane_b32 s0, v1, 0
	s_nop 0
	v_mov_b32_e32 v3, s1
	v_readlane_b32 s1, v1, 48
	v_add_f32_e32 v3, s0, v3
	v_readlane_b32 s0, v1, 32
	v_mov_b32_e32 v1, s1
	s_nop 0
	v_add_f32_e32 v1, s0, v1
	v_add_f32_e32 v1, v3, v1
	v_mov_b32_e32 v3, 0x358637bd
	v_fmac_f32_e32 v3, 0x39800000, v1
	s_mov_b32 s0, 0xf800000
	v_mul_f32_e32 v1, 0x4f800000, v3
	v_cmp_gt_f32_e32 vcc, s0, v3
	s_nop 1
	v_cndmask_b32_e32 v1, v3, v1, vcc
	v_sqrt_f32_e32 v3, v1
	s_nop 0
	v_add_u32_e32 v4, -1, v3
	v_fma_f32 v5, -v4, v3, v1
	v_cmp_ge_f32_e64 s[0:1], 0, v5
	v_add_u32_e32 v5, 1, v3
	s_nop 0
	v_cndmask_b32_e64 v4, v3, v4, s[0:1]
	v_fma_f32 v3, -v5, v3, v1
	v_cmp_lt_f32_e64 s[0:1], 0, v3
	s_nop 1
	v_cndmask_b32_e64 v3, v4, v5, s[0:1]
	v_mul_f32_e32 v4, 0x37800000, v3
	v_cndmask_b32_e32 v3, v3, v4, vcc
	v_mov_b32_e32 v4, 0x260
	v_cmp_class_f32_e32 vcc, v1, v4
	s_nop 1
	v_cndmask_b32_e32 v3, v3, v1, vcc
	v_div_scale_f32 v4, s[0:1], v3, v3, 1.0
	v_rcp_f32_e32 v5, v4
	s_nop 0
	v_fma_f32 v0, -v4, v5, 1.0
	v_fmac_f32_e32 v5, v0, v5
	v_div_scale_f32 v0, vcc, 1.0, v3, 1.0
	v_mul_f32_e32 v2, v0, v5
	v_fma_f32 v8, -v4, v2, v0
	v_fmac_f32_e32 v2, v8, v5
	v_fma_f32 v0, -v4, v2, v0
	v_div_fmas_f32 v0, v0, v5, v2
	v_div_fixup_f32 v2, v0, v3, 1.0
	v_mov_b32_e32 v42, v2
	v_mov_b32_e32 v43, v2
	ds_read_b32 v1, v7 offset:4608
	s_waitcnt lgkmcnt(0)
; __device__ __forceinline__ float rdlane(float v, int l) { return __builtin_bit_cast(float, __builtin_amdgcn_readlane(__builtin_bit_cast(int, v), l)); }
; __device__ __forceinline__ float wave_sum(float v) { v = dpp_add16(v); return (rdlane(v, 0) + rdlane(v, 16)) + (rdlane(v, 32) + rdlane(v, 48)); }
; __device__ __forceinline__ void p12_peer(Frame& F) {
;     ...
;       for (int i = 0; i < 4; ++i) { const int t = F.gw + i * F.NGW;
;           const float rs = 1.0f / sqrtf(wave_sum(SSQ[i * 64 + l2_]) * (1.f / D_) + 1e-6f);
; _Pragma("nounroll")
;           for (int c0 = 0; c0 < 16; c0 += 8) {
; #pragma unroll
;               for (int c = c0; c < c0 + 8; ++c) { const size_t col = (size_t)t * D_ + (size_t)(unsigned)(256 * c + lo2_); const f32x4 gn = *(const f32x4*)(lnf + (256 * c + lo2_));
;                   const f32x4 o = *(const f32x4*)(F.out + col);
;                   *(f32x4*)(F.out + col) = (f32x4){o.x * rs * gn.x, o.y * rs * gn.y, o.z * rs * gn.z, o.w * rs * gn.w}; }
	v_add_f32_dpp v1, v1, v1 quad_perm:[1,0,3,2] row_mask:0xf bank_mask:0xf bound_ctrl:1
	s_nop 1
	v_add_f32_dpp v1, v1, v1 quad_perm:[2,3,0,1] row_mask:0xf bank_mask:0xf bound_ctrl:1
	s_nop 1
	v_add_f32_dpp v1, v1, v1 row_half_mirror row_mask:0xf bank_mask:0xf bound_ctrl:1
	s_nop 1
	v_add_f32_dpp v1, v1, v1 row_mirror row_mask:0xf bank_mask:0xf bound_ctrl:1
	s_nop 0
	v_readlane_b32 s1, v1, 16
	v_readlane_b32 s0, v1, 0
	s_nop 0
	v_mov_b32_e32 v3, s1
	v_readlane_b32 s1, v1, 48
	v_add_f32_e32 v3, s0, v3
	v_readlane_b32 s0, v1, 32
	v_mov_b32_e32 v1, s1
	s_nop 0
	v_add_f32_e32 v1, s0, v1
	v_add_f32_e32 v1, v3, v1
	v_mov_b32_e32 v3, 0x358637bd
	v_fmac_f32_e32 v3, 0x39800000, v1
	s_mov_b32 s0, 0xf800000
	v_mul_f32_e32 v1, 0x4f800000, v3
	v_cmp_gt_f32_e32 vcc, s0, v3
	s_nop 1
	v_cndmask_b32_e32 v1, v3, v1, vcc
	v_sqrt_f32_e32 v3, v1
	s_nop 0
	v_add_u32_e32 v4, -1, v3
	v_fma_f32 v5, -v4, v3, v1
	v_cmp_ge_f32_e64 s[0:1], 0, v5
	v_add_u32_e32 v5, 1, v3
	s_nop 0
	v_cndmask_b32_e64 v4, v3, v4, s[0:1]
	v_fma_f32 v3, -v5, v3, v1
	v_cmp_lt_f32_e64 s[0:1], 0, v3
	s_nop 1
	v_cndmask_b32_e64 v3, v4, v5, s[0:1]
	v_mul_f32_e32 v4, 0x37800000, v3
	v_cndmask_b32_e32 v3, v3, v4, vcc
	v_mov_b32_e32 v4, 0x260
	v_cmp_class_f32_e32 vcc, v1, v4
	s_nop 1
	v_cndmask_b32_e32 v3, v3, v1, vcc
	v_div_scale_f32 v4, s[0:1], v3, v3, 1.0
	v_rcp_f32_e32 v5, v4
	s_nop 0
	v_fma_f32 v0, -v4, v5, 1.0
	v_fmac_f32_e32 v5, v0, v5
	v_div_scale_f32 v0, vcc, 1.0, v3, 1.0
	v_mul_f32_e32 v2, v0, v5
	v_fma_f32 v8, -v4, v2, v0
	v_fmac_f32_e32 v2, v8, v5
	v_fma_f32 v0, -v4, v2, v0
	v_div_fmas_f32 v0, v0, v5, v2
	v_div_fixup_f32 v2, v0, v3, 1.0
	v_mov_b32_e32 v44, v2
	v_mov_b32_e32 v45, v2
	ds_read_b32 v1, v7 offset:4864
	s_waitcnt lgkmcnt(0)
	v_add_f32_dpp v1, v1, v1 quad_perm:[1,0,3,2] row_mask:0xf bank_mask:0xf bound_ctrl:1
	s_nop 1
	v_add_f32_dpp v1, v1, v1 quad_perm:[2,3,0,1] row_mask:0xf bank_mask:0xf bound_ctrl:1
	s_nop 1
	v_add_f32_dpp v1, v1, v1 row_half_mirror row_mask:0xf bank_mask:0xf bound_ctrl:1
	s_nop 1
	v_add_f32_dpp v1, v1, v1 row_mirror row_mask:0xf bank_mask:0xf bound_ctrl:1
	s_nop 0
	v_readlane_b32 s1, v1, 16
	v_readlane_b32 s0, v1, 0
	s_nop 0
	v_mov_b32_e32 v3, s1
	v_readlane_b32 s1, v1, 48
	v_add_f32_e32 v3, s0, v3
	v_readlane_b32 s0, v1, 32
	v_mov_b32_e32 v1, s1
	s_nop 0
	v_add_f32_e32 v1, s0, v1
	v_add_f32_e32 v1, v3, v1
	v_mov_b32_e32 v3, 0x358637bd
	v_fmac_f32_e32 v3, 0x39800000, v1
	s_mov_b32 s0, 0xf800000
	v_mul_f32_e32 v1, 0x4f800000, v3
	v_cmp_gt_f32_e32 vcc, s0, v3
	s_nop 1
	v_cndmask_b32_e32 v1, v3, v1, vcc
	v_sqrt_f32_e32 v3, v1
	s_nop 0
	v_add_u32_e32 v4, -1, v3
	v_fma_f32 v5, -v4, v3, v1
	v_cmp_ge_f32_e64 s[0:1], 0, v5
	v_add_u32_e32 v5, 1, v3
	s_nop 0
	v_cndmask_b32_e64 v4, v3, v4, s[0:1]
	v_fma_f32 v3, -v5, v3, v1
	v_cmp_lt_f32_e64 s[0:1], 0, v3
	s_nop 1
	v_cndmask_b32_e64 v3, v4, v5, s[0:1]
	v_mul_f32_e32 v4, 0x37800000, v3
	v_cndmask_b32_e32 v3, v3, v4, vcc
	v_mov_b32_e32 v4, 0x260
	v_cmp_class_f32_e32 vcc, v1, v4
	s_nop 1
	v_cndmask_b32_e32 v3, v3, v1, vcc
	v_div_scale_f32 v4, s[0:1], v3, v3, 1.0
	v_rcp_f32_e32 v5, v4
	s_nop 0
	v_fma_f32 v0, -v4, v5, 1.0
	v_fmac_f32_e32 v5, v0, v5
	v_div_scale_f32 v0, vcc, 1.0, v3, 1.0
	v_mul_f32_e32 v2, v0, v5
	v_fma_f32 v8, -v4, v2, v0
	v_fmac_f32_e32 v2, v8, v5
	v_fma_f32 v0, -v4, v2, v0
	v_div_fmas_f32 v0, v0, v5, v2
	v_div_fixup_f32 v2, v0, v3, 1.0
	v_mov_b32_e32 v46, v2
	v_mov_b32_e32 v47, v2
	s_waitcnt vmcnt(31)
	v_pk_mul_f32 v[124:125], v[40:41], v[124:125]
	v_pk_mul_f32 v[126:127], v[40:41], v[126:127]
	v_pk_mul_f32 v[124:125], v[60:61], v[124:125]
	v_pk_mul_f32 v[126:127], v[62:63], v[126:127]
	global_store_dwordx4 v6, v[124:127], s[12:13] offset:0
	s_waitcnt vmcnt(31)
	v_pk_mul_f32 v[128:129], v[40:41], v[128:129]
	v_pk_mul_f32 v[130:131], v[40:41], v[130:131]
	v_pk_mul_f32 v[128:129], v[64:65], v[128:129]
	v_pk_mul_f32 v[130:131], v[66:67], v[130:131]
	global_store_dwordx4 v6, v[128:131], s[12:13] offset:1024
	s_waitcnt vmcnt(31)
	v_pk_mul_f32 v[132:133], v[40:41], v[132:133]
	v_pk_mul_f32 v[134:135], v[40:41], v[134:135]
	v_pk_mul_f32 v[132:133], v[68:69], v[132:133]
	v_pk_mul_f32 v[134:135], v[70:71], v[134:135]
	global_store_dwordx4 v6, v[132:135], s[12:13] offset:2048
	s_waitcnt vmcnt(31)
	v_pk_mul_f32 v[136:137], v[40:41], v[136:137]
	v_pk_mul_f32 v[138:139], v[40:41], v[138:139]
	v_pk_mul_f32 v[136:137], v[72:73], v[136:137]
	v_pk_mul_f32 v[138:139], v[74:75], v[138:139]
	global_store_dwordx4 v6, v[136:139], s[12:13] offset:3072
	s_waitcnt vmcnt(31)
	v_pk_mul_f32 v[140:141], v[40:41], v[140:141]
	v_pk_mul_f32 v[142:143], v[40:41], v[142:143]
	v_pk_mul_f32 v[140:141], v[76:77], v[140:141]
	v_pk_mul_f32 v[142:143], v[78:79], v[142:143]
	global_store_dwordx4 v10, v[140:143], s[12:13] offset:0
	s_waitcnt vmcnt(31)
	v_pk_mul_f32 v[144:145], v[40:41], v[144:145]
	v_pk_mul_f32 v[146:147], v[40:41], v[146:147]
	v_pk_mul_f32 v[144:145], v[80:81], v[144:145]
	v_pk_mul_f32 v[146:147], v[82:83], v[146:147]
	global_store_dwordx4 v10, v[144:147], s[12:13] offset:1024
	s_waitcnt vmcnt(31)
	v_pk_mul_f32 v[148:149], v[40:41], v[148:149]
	v_pk_mul_f32 v[150:151], v[40:41], v[150:151]
	v_pk_mul_f32 v[148:149], v[84:85], v[148:149]
	v_pk_mul_f32 v[150:151], v[86:87], v[150:151]
	global_store_dwordx4 v10, v[148:151], s[12:13] offset:2048
	s_waitcnt vmcnt(31)
	v_pk_mul_f32 v[152:153], v[40:41], v[152:153]
	v_pk_mul_f32 v[154:155], v[40:41], v[154:155]
	v_pk_mul_f32 v[152:153], v[88:89], v[152:153]
	v_pk_mul_f32 v[154:155], v[90:91], v[154:155]
	global_store_dwordx4 v10, v[152:155], s[12:13] offset:3072
	s_waitcnt vmcnt(31)
; __device__ __forceinline__ float wave_sum(float v) { v = dpp_add16(v); return (rdlane(v, 0) + rdlane(v, 16)) + (rdlane(v, 32) + rdlane(v, 48)); }
; __device__ __forceinline__ void p12_peer(Frame& F) {
;     ...
;       for (int i = 0; i < 4; ++i) { const int t = F.gw + i * F.NGW;
;           const float rs = 1.0f / sqrtf(wave_sum(SSQ[i * 64 + l2_]) * (1.f / D_) + 1e-6f);
; _Pragma("nounroll")
;           for (int c0 = 0; c0 < 16; c0 += 8) {
; #pragma unroll
;               for (int c = c0; c < c0 + 8; ++c) { const size_t col = (size_t)t * D_ + (size_t)(unsigned)(256 * c + lo2_); const f32x4 gn = *(const f32x4*)(lnf + (256 * c + lo2_));
;                   const f32x4 o = *(const f32x4*)(F.out + col);
;                   *(f32x4*)(F.out + col) = (f32x4){o.x * rs * gn.x, o.y * rs * gn.y, o.z * rs * gn.z, o.w * rs * gn.w}; }
	v_pk_mul_f32 v[156:157], v[40:41], v[156:157]
	v_pk_mul_f32 v[158:159], v[40:41], v[158:159]
	v_pk_mul_f32 v[156:157], v[92:93], v[156:157]
	v_pk_mul_f32 v[158:159], v[94:95], v[158:159]
	global_store_dwordx4 v11, v[156:159], s[12:13] offset:0
	s_waitcnt vmcnt(31)
	v_pk_mul_f32 v[160:161], v[40:41], v[160:161]
	v_pk_mul_f32 v[162:163], v[40:41], v[162:163]
	v_pk_mul_f32 v[160:161], v[96:97], v[160:161]
	v_pk_mul_f32 v[162:163], v[98:99], v[162:163]
	global_store_dwordx4 v11, v[160:163], s[12:13] offset:1024
	s_waitcnt vmcnt(31)
	v_pk_mul_f32 v[164:165], v[40:41], v[164:165]
	v_pk_mul_f32 v[166:167], v[40:41], v[166:167]
	v_pk_mul_f32 v[164:165], v[100:101], v[164:165]
	v_pk_mul_f32 v[166:167], v[102:103], v[166:167]
	global_store_dwordx4 v11, v[164:167], s[12:13] offset:2048
	s_waitcnt vmcnt(31)
	v_pk_mul_f32 v[168:169], v[40:41], v[168:169]
	v_pk_mul_f32 v[170:171], v[40:41], v[170:171]
	v_pk_mul_f32 v[168:169], v[104:105], v[168:169]
	v_pk_mul_f32 v[170:171], v[106:107], v[170:171]
	global_store_dwordx4 v11, v[168:171], s[12:13] offset:3072
	s_waitcnt vmcnt(31)
	v_pk_mul_f32 v[172:173], v[40:41], v[172:173]
	v_pk_mul_f32 v[174:175], v[40:41], v[174:175]
	v_pk_mul_f32 v[172:173], v[108:109], v[172:173]
	v_pk_mul_f32 v[174:175], v[110:111], v[174:175]
	global_store_dwordx4 v12, v[172:175], s[12:13] offset:0
	s_waitcnt vmcnt(31)
	v_pk_mul_f32 v[176:177], v[40:41], v[176:177]
	v_pk_mul_f32 v[178:179], v[40:41], v[178:179]
	v_pk_mul_f32 v[176:177], v[112:113], v[176:177]
	v_pk_mul_f32 v[178:179], v[114:115], v[178:179]
	global_store_dwordx4 v12, v[176:179], s[12:13] offset:1024
	s_waitcnt vmcnt(31)
	v_pk_mul_f32 v[180:181], v[40:41], v[180:181]
	v_pk_mul_f32 v[182:183], v[40:41], v[182:183]
	v_pk_mul_f32 v[180:181], v[116:117], v[180:181]
	v_pk_mul_f32 v[182:183], v[118:119], v[182:183]
	global_store_dwordx4 v12, v[180:183], s[12:13] offset:2048
	s_waitcnt vmcnt(31)
	v_pk_mul_f32 v[184:185], v[40:41], v[184:185]
	v_pk_mul_f32 v[186:187], v[40:41], v[186:187]
	v_pk_mul_f32 v[184:185], v[120:121], v[184:185]
	v_pk_mul_f32 v[186:187], v[122:123], v[186:187]
	global_store_dwordx4 v12, v[184:187], s[12:13] offset:3072
	s_nop 1
	global_load_dwordx4 v[124:127], v6, s[16:17] offset:0
	global_load_dwordx4 v[128:131], v6, s[16:17] offset:1024
	global_load_dwordx4 v[132:135], v6, s[16:17] offset:2048
	global_load_dwordx4 v[136:139], v6, s[16:17] offset:3072
	global_load_dwordx4 v[140:143], v10, s[16:17] offset:0
	global_load_dwordx4 v[144:147], v10, s[16:17] offset:1024
	global_load_dwordx4 v[148:151], v10, s[16:17] offset:2048
	global_load_dwordx4 v[152:155], v10, s[16:17] offset:3072
	global_load_dwordx4 v[156:159], v11, s[16:17] offset:0
	global_load_dwordx4 v[160:163], v11, s[16:17] offset:1024
	global_load_dwordx4 v[164:167], v11, s[16:17] offset:2048
	global_load_dwordx4 v[168:171], v11, s[16:17] offset:3072
	global_load_dwordx4 v[172:175], v12, s[16:17] offset:0
	global_load_dwordx4 v[176:179], v12, s[16:17] offset:1024
	global_load_dwordx4 v[180:183], v12, s[16:17] offset:2048
	global_load_dwordx4 v[184:187], v12, s[16:17] offset:3072
	s_waitcnt vmcnt(47)
	v_pk_mul_f32 v[188:189], v[42:43], v[188:189]
	v_pk_mul_f32 v[190:191], v[42:43], v[190:191]
	v_pk_mul_f32 v[188:189], v[60:61], v[188:189]
	v_pk_mul_f32 v[190:191], v[62:63], v[190:191]
	global_store_dwordx4 v6, v[188:191], s[14:15] offset:0
	s_waitcnt vmcnt(47)
	v_pk_mul_f32 v[192:193], v[42:43], v[192:193]
	v_pk_mul_f32 v[194:195], v[42:43], v[194:195]
	v_pk_mul_f32 v[192:193], v[64:65], v[192:193]
	v_pk_mul_f32 v[194:195], v[66:67], v[194:195]
	global_store_dwordx4 v6, v[192:195], s[14:15] offset:1024
	s_waitcnt vmcnt(47)
	v_pk_mul_f32 v[196:197], v[42:43], v[196:197]
	v_pk_mul_f32 v[198:199], v[42:43], v[198:199]
	v_pk_mul_f32 v[196:197], v[68:69], v[196:197]
	v_pk_mul_f32 v[198:199], v[70:71], v[198:199]
	global_store_dwordx4 v6, v[196:199], s[14:15] offset:2048
	s_waitcnt vmcnt(47)
	v_pk_mul_f32 v[200:201], v[42:43], v[200:201]
	v_pk_mul_f32 v[202:203], v[42:43], v[202:203]
	v_pk_mul_f32 v[200:201], v[72:73], v[200:201]
	v_pk_mul_f32 v[202:203], v[74:75], v[202:203]
	global_store_dwordx4 v6, v[200:203], s[14:15] offset:3072
	s_waitcnt vmcnt(47)
	v_pk_mul_f32 v[204:205], v[42:43], v[204:205]
	v_pk_mul_f32 v[206:207], v[42:43], v[206:207]
	v_pk_mul_f32 v[204:205], v[76:77], v[204:205]
	v_pk_mul_f32 v[206:207], v[78:79], v[206:207]
	global_store_dwordx4 v10, v[204:207], s[14:15] offset:0
	s_waitcnt vmcnt(47)
	v_pk_mul_f32 v[208:209], v[42:43], v[208:209]
	v_pk_mul_f32 v[210:211], v[42:43], v[210:211]
	v_pk_mul_f32 v[208:209], v[80:81], v[208:209]
	v_pk_mul_f32 v[210:211], v[82:83], v[210:211]
	global_store_dwordx4 v10, v[208:211], s[14:15] offset:1024
	s_waitcnt vmcnt(47)
	v_pk_mul_f32 v[212:213], v[42:43], v[212:213]
	v_pk_mul_f32 v[214:215], v[42:43], v[214:215]
	v_pk_mul_f32 v[212:213], v[84:85], v[212:213]
	v_pk_mul_f32 v[214:215], v[86:87], v[214:215]
	global_store_dwordx4 v10, v[212:215], s[14:15] offset:2048
	s_waitcnt vmcnt(47)
	v_pk_mul_f32 v[216:217], v[42:43], v[216:217]
	v_pk_mul_f32 v[218:219], v[42:43], v[218:219]
	v_pk_mul_f32 v[216:217], v[88:89], v[216:217]
	v_pk_mul_f32 v[218:219], v[90:91], v[218:219]
	global_store_dwordx4 v10, v[216:219], s[14:15] offset:3072
	s_waitcnt vmcnt(47)
	v_pk_mul_f32 v[220:221], v[42:43], v[220:221]
	v_pk_mul_f32 v[222:223], v[42:43], v[222:223]
	v_pk_mul_f32 v[220:221], v[92:93], v[220:221]
	v_pk_mul_f32 v[222:223], v[94:95], v[222:223]
	global_store_dwordx4 v11, v[220:223], s[14:15] offset:0
	s_waitcnt vmcnt(47)
; __device__ __forceinline__ float wave_sum(float v) { v = dpp_add16(v); return (rdlane(v, 0) + rdlane(v, 16)) + (rdlane(v, 32) + rdlane(v, 48)); }
; __device__ __forceinline__ void p12_peer(Frame& F) {
;     ...
;       for (int i = 0; i < 4; ++i) { const int t = F.gw + i * F.NGW;
;           const float rs = 1.0f / sqrtf(wave_sum(SSQ[i * 64 + l2_]) * (1.f / D_) + 1e-6f);
; _Pragma("nounroll")
;           for (int c0 = 0; c0 < 16; c0 += 8) {
; #pragma unroll
;               for (int c = c0; c < c0 + 8; ++c) { const size_t col = (size_t)t * D_ + (size_t)(unsigned)(256 * c + lo2_); const f32x4 gn = *(const f32x4*)(lnf + (256 * c + lo2_));
;                   const f32x4 o = *(const f32x4*)(F.out + col);
;                   *(f32x4*)(F.out + col) = (f32x4){o.x * rs * gn.x, o.y * rs * gn.y, o.z * rs * gn.z, o.w * rs * gn.w}; }
	v_pk_mul_f32 v[224:225], v[42:43], v[224:225]
	v_pk_mul_f32 v[226:227], v[42:43], v[226:227]
	v_pk_mul_f32 v[224:225], v[96:97], v[224:225]
	v_pk_mul_f32 v[226:227], v[98:99], v[226:227]
	global_store_dwordx4 v11, v[224:227], s[14:15] offset:1024
	s_waitcnt vmcnt(47)
	v_pk_mul_f32 v[228:229], v[42:43], v[228:229]
	v_pk_mul_f32 v[230:231], v[42:43], v[230:231]
	v_pk_mul_f32 v[228:229], v[100:101], v[228:229]
	v_pk_mul_f32 v[230:231], v[102:103], v[230:231]
	global_store_dwordx4 v11, v[228:231], s[14:15] offset:2048
	s_waitcnt vmcnt(47)
	v_pk_mul_f32 v[232:233], v[42:43], v[232:233]
	v_pk_mul_f32 v[234:235], v[42:43], v[234:235]
	v_pk_mul_f32 v[232:233], v[104:105], v[232:233]
	v_pk_mul_f32 v[234:235], v[106:107], v[234:235]
	global_store_dwordx4 v11, v[232:235], s[14:15] offset:3072
	s_waitcnt vmcnt(47)
	v_pk_mul_f32 v[236:237], v[42:43], v[236:237]
	v_pk_mul_f32 v[238:239], v[42:43], v[238:239]
	v_pk_mul_f32 v[236:237], v[108:109], v[236:237]
	v_pk_mul_f32 v[238:239], v[110:111], v[238:239]
	global_store_dwordx4 v12, v[236:239], s[14:15] offset:0
	s_waitcnt vmcnt(47)
	v_pk_mul_f32 v[240:241], v[42:43], v[240:241]
	v_pk_mul_f32 v[242:243], v[42:43], v[242:243]
	v_pk_mul_f32 v[240:241], v[112:113], v[240:241]
	v_pk_mul_f32 v[242:243], v[114:115], v[242:243]
	global_store_dwordx4 v12, v[240:243], s[14:15] offset:1024
	s_waitcnt vmcnt(47)
	v_pk_mul_f32 v[244:245], v[42:43], v[244:245]
	v_pk_mul_f32 v[246:247], v[42:43], v[246:247]
	v_pk_mul_f32 v[244:245], v[116:117], v[244:245]
	v_pk_mul_f32 v[246:247], v[118:119], v[246:247]
	global_store_dwordx4 v12, v[244:247], s[14:15] offset:2048
	s_waitcnt vmcnt(47)
	v_pk_mul_f32 v[248:249], v[42:43], v[248:249]
	v_pk_mul_f32 v[250:251], v[42:43], v[250:251]
	v_pk_mul_f32 v[248:249], v[120:121], v[248:249]
	v_pk_mul_f32 v[250:251], v[122:123], v[250:251]
	global_store_dwordx4 v12, v[248:251], s[14:15] offset:3072
	s_nop 1
	global_load_dwordx4 v[188:191], v6, s[18:19] offset:0
	global_load_dwordx4 v[192:195], v6, s[18:19] offset:1024
	global_load_dwordx4 v[196:199], v6, s[18:19] offset:2048
	global_load_dwordx4 v[200:203], v6, s[18:19] offset:3072
	global_load_dwordx4 v[204:207], v10, s[18:19] offset:0
	global_load_dwordx4 v[208:211], v10, s[18:19] offset:1024
	global_load_dwordx4 v[212:215], v10, s[18:19] offset:2048
	global_load_dwordx4 v[216:219], v10, s[18:19] offset:3072
	global_load_dwordx4 v[220:223], v11, s[18:19] offset:0
	global_load_dwordx4 v[224:227], v11, s[18:19] offset:1024
	global_load_dwordx4 v[228:231], v11, s[18:19] offset:2048
	global_load_dwordx4 v[232:235], v11, s[18:19] offset:3072
	global_load_dwordx4 v[236:239], v12, s[18:19] offset:0
	global_load_dwordx4 v[240:243], v12, s[18:19] offset:1024
	global_load_dwordx4 v[244:247], v12, s[18:19] offset:2048
	global_load_dwordx4 v[248:251], v12, s[18:19] offset:3072
	s_waitcnt vmcnt(47)
	v_pk_mul_f32 v[124:125], v[44:45], v[124:125]
	v_pk_mul_f32 v[126:127], v[44:45], v[126:127]
	v_pk_mul_f32 v[124:125], v[60:61], v[124:125]
	v_pk_mul_f32 v[126:127], v[62:63], v[126:127]
	global_store_dwordx4 v6, v[124:127], s[16:17] offset:0
	s_waitcnt vmcnt(47)
	v_pk_mul_f32 v[128:129], v[44:45], v[128:129]
	v_pk_mul_f32 v[130:131], v[44:45], v[130:131]
	v_pk_mul_f32 v[128:129], v[64:65], v[128:129]
	v_pk_mul_f32 v[130:131], v[66:67], v[130:131]
	global_store_dwordx4 v6, v[128:131], s[16:17] offset:1024
	s_waitcnt vmcnt(47)
	v_pk_mul_f32 v[132:133], v[44:45], v[132:133]
	v_pk_mul_f32 v[134:135], v[44:45], v[134:135]
	v_pk_mul_f32 v[132:133], v[68:69], v[132:133]
	v_pk_mul_f32 v[134:135], v[70:71], v[134:135]
	global_store_dwordx4 v6, v[132:135], s[16:17] offset:2048
	s_waitcnt vmcnt(47)
	v_pk_mul_f32 v[136:137], v[44:45], v[136:137]
	v_pk_mul_f32 v[138:139], v[44:45], v[138:139]
	v_pk_mul_f32 v[136:137], v[72:73], v[136:137]
	v_pk_mul_f32 v[138:139], v[74:75], v[138:139]
	global_store_dwordx4 v6, v[136:139], s[16:17] offset:3072
	s_waitcnt vmcnt(47)
	v_pk_mul_f32 v[140:141], v[44:45], v[140:141]
	v_pk_mul_f32 v[142:143], v[44:45], v[142:143]
	v_pk_mul_f32 v[140:141], v[76:77], v[140:141]
	v_pk_mul_f32 v[142:143], v[78:79], v[142:143]
	global_store_dwordx4 v10, v[140:143], s[16:17] offset:0
	s_waitcnt vmcnt(47)
	v_pk_mul_f32 v[144:145], v[44:45], v[144:145]
	v_pk_mul_f32 v[146:147], v[44:45], v[146:147]
	v_pk_mul_f32 v[144:145], v[80:81], v[144:145]
	v_pk_mul_f32 v[146:147], v[82:83], v[146:147]
	global_store_dwordx4 v10, v[144:147], s[16:17] offset:1024
	s_waitcnt vmcnt(47)
	v_pk_mul_f32 v[148:149], v[44:45], v[148:149]
	v_pk_mul_f32 v[150:151], v[44:45], v[150:151]
	v_pk_mul_f32 v[148:149], v[84:85], v[148:149]
	v_pk_mul_f32 v[150:151], v[86:87], v[150:151]
	global_store_dwordx4 v10, v[148:151], s[16:17] offset:2048
	s_waitcnt vmcnt(47)
	v_pk_mul_f32 v[152:153], v[44:45], v[152:153]
	v_pk_mul_f32 v[154:155], v[44:45], v[154:155]
	v_pk_mul_f32 v[152:153], v[88:89], v[152:153]
	v_pk_mul_f32 v[154:155], v[90:91], v[154:155]
	global_store_dwordx4 v10, v[152:155], s[16:17] offset:3072
	s_waitcnt vmcnt(47)
	v_pk_mul_f32 v[156:157], v[44:45], v[156:157]
	v_pk_mul_f32 v[158:159], v[44:45], v[158:159]
	v_pk_mul_f32 v[156:157], v[92:93], v[156:157]
	v_pk_mul_f32 v[158:159], v[94:95], v[158:159]
	global_store_dwordx4 v11, v[156:159], s[16:17] offset:0
	s_waitcnt vmcnt(47)
	v_pk_mul_f32 v[160:161], v[44:45], v[160:161]
	v_pk_mul_f32 v[162:163], v[44:45], v[162:163]
	v_pk_mul_f32 v[160:161], v[96:97], v[160:161]
	v_pk_mul_f32 v[162:163], v[98:99], v[162:163]
	global_store_dwordx4 v11, v[160:163], s[16:17] offset:1024
	s_waitcnt vmcnt(47)
; __device__ __forceinline__ float wave_sum(float v) { v = dpp_add16(v); return (rdlane(v, 0) + rdlane(v, 16)) + (rdlane(v, 32) + rdlane(v, 48)); }
; __device__ __forceinline__ void p12_peer(Frame& F) {
;     ...
;       for (int i = 0; i < 4; ++i) { const int t = F.gw + i * F.NGW;
;           const float rs = 1.0f / sqrtf(wave_sum(SSQ[i * 64 + l2_]) * (1.f / D_) + 1e-6f);
; _Pragma("nounroll")
;           for (int c0 = 0; c0 < 16; c0 += 8) {
; #pragma unroll
;               for (int c = c0; c < c0 + 8; ++c) { const size_t col = (size_t)t * D_ + (size_t)(unsigned)(256 * c + lo2_); const f32x4 gn = *(const f32x4*)(lnf + (256 * c + lo2_));
;                   const f32x4 o = *(const f32x4*)(F.out + col);
;                   *(f32x4*)(F.out + col) = (f32x4){o.x * rs * gn.x, o.y * rs * gn.y, o.z * rs * gn.z, o.w * rs * gn.w}; }
	v_pk_mul_f32 v[164:165], v[44:45], v[164:165]
	v_pk_mul_f32 v[166:167], v[44:45], v[166:167]
	v_pk_mul_f32 v[164:165], v[100:101], v[164:165]
	v_pk_mul_f32 v[166:167], v[102:103], v[166:167]
	global_store_dwordx4 v11, v[164:167], s[16:17] offset:2048
	s_waitcnt vmcnt(47)
	v_pk_mul_f32 v[168:169], v[44:45], v[168:169]
	v_pk_mul_f32 v[170:171], v[44:45], v[170:171]
	v_pk_mul_f32 v[168:169], v[104:105], v[168:169]
	v_pk_mul_f32 v[170:171], v[106:107], v[170:171]
	global_store_dwordx4 v11, v[168:171], s[16:17] offset:3072
	s_waitcnt vmcnt(47)
	v_pk_mul_f32 v[172:173], v[44:45], v[172:173]
	v_pk_mul_f32 v[174:175], v[44:45], v[174:175]
	v_pk_mul_f32 v[172:173], v[108:109], v[172:173]
	v_pk_mul_f32 v[174:175], v[110:111], v[174:175]
	global_store_dwordx4 v12, v[172:175], s[16:17] offset:0
	s_waitcnt vmcnt(47)
	v_pk_mul_f32 v[176:177], v[44:45], v[176:177]
	v_pk_mul_f32 v[178:179], v[44:45], v[178:179]
	v_pk_mul_f32 v[176:177], v[112:113], v[176:177]
	v_pk_mul_f32 v[178:179], v[114:115], v[178:179]
	global_store_dwordx4 v12, v[176:179], s[16:17] offset:1024
	s_waitcnt vmcnt(47)
	v_pk_mul_f32 v[180:181], v[44:45], v[180:181]
	v_pk_mul_f32 v[182:183], v[44:45], v[182:183]
	v_pk_mul_f32 v[180:181], v[116:117], v[180:181]
	v_pk_mul_f32 v[182:183], v[118:119], v[182:183]
	global_store_dwordx4 v12, v[180:183], s[16:17] offset:2048
	s_waitcnt vmcnt(47)
	v_pk_mul_f32 v[184:185], v[44:45], v[184:185]
	v_pk_mul_f32 v[186:187], v[44:45], v[186:187]
	v_pk_mul_f32 v[184:185], v[120:121], v[184:185]
	v_pk_mul_f32 v[186:187], v[122:123], v[186:187]
	global_store_dwordx4 v12, v[184:187], s[16:17] offset:3072
	s_waitcnt vmcnt(31)
	v_pk_mul_f32 v[188:189], v[46:47], v[188:189]
	v_pk_mul_f32 v[190:191], v[46:47], v[190:191]
	v_pk_mul_f32 v[188:189], v[60:61], v[188:189]
	v_pk_mul_f32 v[190:191], v[62:63], v[190:191]
	global_store_dwordx4 v6, v[188:191], s[18:19] offset:0
	s_waitcnt vmcnt(31)
	v_pk_mul_f32 v[192:193], v[46:47], v[192:193]
	v_pk_mul_f32 v[194:195], v[46:47], v[194:195]
	v_pk_mul_f32 v[192:193], v[64:65], v[192:193]
	v_pk_mul_f32 v[194:195], v[66:67], v[194:195]
	global_store_dwordx4 v6, v[192:195], s[18:19] offset:1024
	s_waitcnt vmcnt(31)
	v_pk_mul_f32 v[196:197], v[46:47], v[196:197]
	v_pk_mul_f32 v[198:199], v[46:47], v[198:199]
	v_pk_mul_f32 v[196:197], v[68:69], v[196:197]
	v_pk_mul_f32 v[198:199], v[70:71], v[198:199]
	global_store_dwordx4 v6, v[196:199], s[18:19] offset:2048
	s_waitcnt vmcnt(31)
	v_pk_mul_f32 v[200:201], v[46:47], v[200:201]
	v_pk_mul_f32 v[202:203], v[46:47], v[202:203]
	v_pk_mul_f32 v[200:201], v[72:73], v[200:201]
	v_pk_mul_f32 v[202:203], v[74:75], v[202:203]
	global_store_dwordx4 v6, v[200:203], s[18:19] offset:3072
	s_waitcnt vmcnt(31)
	v_pk_mul_f32 v[204:205], v[46:47], v[204:205]
	v_pk_mul_f32 v[206:207], v[46:47], v[206:207]
	v_pk_mul_f32 v[204:205], v[76:77], v[204:205]
	v_pk_mul_f32 v[206:207], v[78:79], v[206:207]
	global_store_dwordx4 v10, v[204:207], s[18:19] offset:0
	s_waitcnt vmcnt(31)
	v_pk_mul_f32 v[208:209], v[46:47], v[208:209]
	v_pk_mul_f32 v[210:211], v[46:47], v[210:211]
	v_pk_mul_f32 v[208:209], v[80:81], v[208:209]
	v_pk_mul_f32 v[210:211], v[82:83], v[210:211]
	global_store_dwordx4 v10, v[208:211], s[18:19] offset:1024
	s_waitcnt vmcnt(31)
	v_pk_mul_f32 v[212:213], v[46:47], v[212:213]
	v_pk_mul_f32 v[214:215], v[46:47], v[214:215]
	v_pk_mul_f32 v[212:213], v[84:85], v[212:213]
	v_pk_mul_f32 v[214:215], v[86:87], v[214:215]
	global_store_dwordx4 v10, v[212:215], s[18:19] offset:2048
	s_waitcnt vmcnt(31)
	v_pk_mul_f32 v[216:217], v[46:47], v[216:217]
	v_pk_mul_f32 v[218:219], v[46:47], v[218:219]
	v_pk_mul_f32 v[216:217], v[88:89], v[216:217]
	v_pk_mul_f32 v[218:219], v[90:91], v[218:219]
	global_store_dwordx4 v10, v[216:219], s[18:19] offset:3072
	s_waitcnt vmcnt(31)
	v_pk_mul_f32 v[220:221], v[46:47], v[220:221]
	v_pk_mul_f32 v[222:223], v[46:47], v[222:223]
	v_pk_mul_f32 v[220:221], v[92:93], v[220:221]
	v_pk_mul_f32 v[222:223], v[94:95], v[222:223]
	global_store_dwordx4 v11, v[220:223], s[18:19] offset:0
	s_waitcnt vmcnt(31)
	v_pk_mul_f32 v[224:225], v[46:47], v[224:225]
	v_pk_mul_f32 v[226:227], v[46:47], v[226:227]
	v_pk_mul_f32 v[224:225], v[96:97], v[224:225]
	v_pk_mul_f32 v[226:227], v[98:99], v[226:227]
	global_store_dwordx4 v11, v[224:227], s[18:19] offset:1024
	s_waitcnt vmcnt(31)
	v_pk_mul_f32 v[228:229], v[46:47], v[228:229]
	v_pk_mul_f32 v[230:231], v[46:47], v[230:231]
	v_pk_mul_f32 v[228:229], v[100:101], v[228:229]
	v_pk_mul_f32 v[230:231], v[102:103], v[230:231]
	global_store_dwordx4 v11, v[228:231], s[18:19] offset:2048
	s_waitcnt vmcnt(31)
	v_pk_mul_f32 v[232:233], v[46:47], v[232:233]
	v_pk_mul_f32 v[234:235], v[46:47], v[234:235]
	v_pk_mul_f32 v[232:233], v[104:105], v[232:233]
	v_pk_mul_f32 v[234:235], v[106:107], v[234:235]
	global_store_dwordx4 v11, v[232:235], s[18:19] offset:3072
	s_waitcnt vmcnt(31)
	v_pk_mul_f32 v[236:237], v[46:47], v[236:237]
	v_pk_mul_f32 v[238:239], v[46:47], v[238:239]
	v_pk_mul_f32 v[236:237], v[108:109], v[236:237]
	v_pk_mul_f32 v[238:239], v[110:111], v[238:239]
	global_store_dwordx4 v12, v[236:239], s[18:19] offset:0
	s_waitcnt vmcnt(31)
	v_pk_mul_f32 v[240:241], v[46:47], v[240:241]
	v_pk_mul_f32 v[242:243], v[46:47], v[242:243]
	v_pk_mul_f32 v[240:241], v[112:113], v[240:241]
	v_pk_mul_f32 v[242:243], v[114:115], v[242:243]
	global_store_dwordx4 v12, v[240:243], s[18:19] offset:1024
	s_waitcnt vmcnt(31)
	v_pk_mul_f32 v[244:245], v[46:47], v[244:245]
	v_pk_mul_f32 v[246:247], v[46:47], v[246:247]
	v_pk_mul_f32 v[244:245], v[116:117], v[244:245]
	v_pk_mul_f32 v[246:247], v[118:119], v[246:247]
	global_store_dwordx4 v12, v[244:247], s[18:19] offset:2048
	s_waitcnt vmcnt(31)
	v_pk_mul_f32 v[248:249], v[46:47], v[248:249]
	v_pk_mul_f32 v[250:251], v[46:47], v[250:251]
	v_pk_mul_f32 v[248:249], v[120:121], v[248:249]
	v_pk_mul_f32 v[250:251], v[122:123], v[250:251]
	global_store_dwordx4 v12, v[248:251], s[18:19] offset:3072
